# v51: v48 + diff epilogue stash loads and LDS output reads batched into dead K-fragment registers; down-GEMM and in-proj epilogue first loads issued before the realign barrier
# baseline (speedup 1.0000x reference)
.LBB0_775:
	s_add_u32 s28, s8, 0xfffe0080
	s_addc_u32 s29, s9, -1
	s_add_i32 s43, 0, 0x10000
	s_cmp_eq_u32 s68, 4
	s_cselect_b32 s29, s3, s29
	s_cselect_b32 s28, s2, s28
	v_add_u32_e32 v0, s43, v198
	s_cselect_b32 s31, s64, s67
	s_cselect_b32 s30, s65, s66
	s_add_i32 s44, 0, 0x14000
	ds_read_b128 v[114:117], v0
	ds_read_b128 v[118:121], v0 offset:1024
	ds_read_b128 v[138:141], v0 offset:2048
	ds_read_b128 v[142:145], v0 offset:3072
	v_add_u32_e32 v0, s44, v198
	ds_read_b128 v[146:149], v0
	ds_read_b128 v[150:153], v0 offset:1024
	ds_read_b128 v[154:157], v0 offset:2048
	ds_read_b128 v[158:161], v0 offset:3072
	s_add_i32 s45, s85, 0xc000
	ds_read_b128 v[162:165], v199
	ds_read_b128 v[166:169], v199 offset:1024
	ds_read_b128 v[170:173], v199 offset:2048
	ds_read_b128 v[174:177], v199 offset:3072
	ds_read_b128 v[178:181], v199 offset:4096
	ds_read_b128 v[182:185], v199 offset:5120
	ds_read_b128 v[186:189], v199 offset:6144
	ds_read_b128 v[190:193], v199 offset:7168
	s_mov_b32 m0, s45
	s_add_i32 s46, s85, 0xe000
	global_load_lds_dwordx4 v194, s[8:9]
	s_mov_b32 m0, s46
	s_nop 0
	global_load_lds_dwordx4 v196, s[8:9]
	s_waitcnt vmcnt(8)
	s_waitcnt lgkmcnt(0)
	s_barrier
	s_setprio 1
	s_waitcnt lgkmcnt(0)
	v_mfma_i32_16x16x64_i8 v[134:137], v[114:117], v[162:165], v[134:137]
	v_mfma_i32_16x16x64_i8 v[130:133], v[138:141], v[162:165], v[130:133]
	v_mfma_i32_16x16x64_i8 v[126:129], v[114:117], v[170:173], v[126:129]
	v_mfma_i32_16x16x64_i8 v[122:125], v[138:141], v[170:173], v[122:125]
	v_mfma_i32_16x16x64_i8 v[110:113], v[114:117], v[178:181], v[110:113]
	v_mfma_i32_16x16x64_i8 v[106:109], v[138:141], v[178:181], v[106:109]
	v_mfma_i32_16x16x64_i8 v[102:105], v[114:117], v[186:189], v[102:105]
	v_mfma_i32_16x16x64_i8 v[98:101], v[138:141], v[186:189], v[98:101]
	v_mfma_i32_16x16x64_i8 v[134:137], v[118:121], v[166:169], v[134:137]
	v_mfma_i32_16x16x64_i8 v[130:133], v[142:145], v[166:169], v[130:133]
	v_mfma_i32_16x16x64_i8 v[126:129], v[118:121], v[174:177], v[126:129]
	v_mfma_i32_16x16x64_i8 v[122:125], v[142:145], v[174:177], v[122:125]
	v_mfma_i32_16x16x64_i8 v[110:113], v[118:121], v[182:185], v[110:113]
	v_mfma_i32_16x16x64_i8 v[106:109], v[142:145], v[182:185], v[106:109]
	v_mfma_i32_16x16x64_i8 v[102:105], v[118:121], v[190:193], v[102:105]
	v_mfma_i32_16x16x64_i8 v[98:101], v[142:145], v[190:193], v[98:101]
	s_setprio 0
	s_setprio 1
	v_mfma_i32_16x16x64_i8 v[62:65], v[146:149], v[162:165], v[62:65]
	v_mfma_i32_16x16x64_i8 v[58:61], v[154:157], v[162:165], v[58:61]
	v_mfma_i32_16x16x64_i8 v[54:57], v[146:149], v[170:173], v[54:57]
	v_mfma_i32_16x16x64_i8 v[50:53], v[154:157], v[170:173], v[50:53]
	v_mfma_i32_16x16x64_i8 v[46:49], v[146:149], v[178:181], v[46:49]
	v_mfma_i32_16x16x64_i8 v[42:45], v[154:157], v[178:181], v[42:45]
	v_mfma_i32_16x16x64_i8 v[38:41], v[146:149], v[186:189], v[38:41]
	v_mfma_i32_16x16x64_i8 v[34:37], v[154:157], v[186:189], v[34:37]
	v_mfma_i32_16x16x64_i8 v[62:65], v[150:153], v[166:169], v[62:65]
	v_mfma_i32_16x16x64_i8 v[58:61], v[158:161], v[166:169], v[58:61]
	v_mfma_i32_16x16x64_i8 v[54:57], v[150:153], v[174:177], v[54:57]
	v_mfma_i32_16x16x64_i8 v[50:53], v[158:161], v[174:177], v[50:53]
	v_mfma_i32_16x16x64_i8 v[46:49], v[150:153], v[182:185], v[46:49]
	v_mfma_i32_16x16x64_i8 v[42:45], v[158:161], v[182:185], v[42:45]
	v_mfma_i32_16x16x64_i8 v[38:41], v[150:153], v[190:193], v[38:41]
	v_mfma_i32_16x16x64_i8 v[34:37], v[158:161], v[190:193], v[34:37]
	s_setprio 0
	s_barrier
	s_add_i32 s47, s43, s33
	ds_read_b128 v[162:165], v199 offset:16384
	ds_read_b128 v[166:169], v199 offset:17408
	ds_read_b128 v[170:173], v199 offset:18432
	ds_read_b128 v[174:177], v199 offset:19456
	ds_read_b128 v[178:181], v199 offset:20480
	ds_read_b128 v[182:185], v199 offset:21504
	ds_read_b128 v[186:189], v199 offset:22528
	ds_read_b128 v[190:193], v199 offset:23552
	s_mov_b32 m0, s47
	s_add_i32 s48, s47, 0x2000
	global_load_lds_dwordx4 v195, s[30:31]
	s_mov_b32 m0, s48
	s_add_u32 s52, s30, 0x20000
	global_load_lds_dwordx4 v197, s[30:31]
	s_addc_u32 s53, s31, 0
	s_add_i32 s49, s44, s33
	s_mov_b32 m0, s49
	s_add_i32 s50, s49, 0x2000
	global_load_lds_dwordx4 v195, s[52:53]
	s_mov_b32 m0, s50
	s_nop 0
	global_load_lds_dwordx4 v197, s[52:53]
	s_waitcnt vmcnt(6)
	s_waitcnt lgkmcnt(0)
	s_barrier
	s_setprio 1
	s_waitcnt lgkmcnt(0)
	v_mfma_i32_16x16x64_i8 v[94:97], v[114:117], v[162:165], v[94:97]
	v_mfma_i32_16x16x64_i8 v[90:93], v[138:141], v[162:165], v[90:93]
	v_mfma_i32_16x16x64_i8 v[86:89], v[114:117], v[170:173], v[86:89]
	v_mfma_i32_16x16x64_i8 v[82:85], v[138:141], v[170:173], v[82:85]
	v_mfma_i32_16x16x64_i8 v[78:81], v[114:117], v[178:181], v[78:81]
	v_mfma_i32_16x16x64_i8 v[74:77], v[138:141], v[178:181], v[74:77]
	v_mfma_i32_16x16x64_i8 v[70:73], v[114:117], v[186:189], v[70:73]
	v_mfma_i32_16x16x64_i8 v[66:69], v[138:141], v[186:189], v[66:69]
	v_mfma_i32_16x16x64_i8 v[94:97], v[118:121], v[166:169], v[94:97]
	v_mfma_i32_16x16x64_i8 v[90:93], v[142:145], v[166:169], v[90:93]
	v_mfma_i32_16x16x64_i8 v[86:89], v[118:121], v[174:177], v[86:89]
	v_mfma_i32_16x16x64_i8 v[82:85], v[142:145], v[174:177], v[82:85]
	v_mfma_i32_16x16x64_i8 v[78:81], v[118:121], v[182:185], v[78:81]
	v_mfma_i32_16x16x64_i8 v[74:77], v[142:145], v[182:185], v[74:77]
	v_mfma_i32_16x16x64_i8 v[70:73], v[118:121], v[190:193], v[70:73]
	v_mfma_i32_16x16x64_i8 v[66:69], v[142:145], v[190:193], v[66:69]
	s_setprio 0
	s_setprio 1
	v_mfma_i32_16x16x64_i8 v[30:33], v[146:149], v[162:165], v[30:33]
	v_mfma_i32_16x16x64_i8 v[26:29], v[154:157], v[162:165], v[26:29]
	v_mfma_i32_16x16x64_i8 v[22:25], v[146:149], v[170:173], v[22:25]
	v_mfma_i32_16x16x64_i8 v[18:21], v[154:157], v[170:173], v[18:21]
	v_mfma_i32_16x16x64_i8 v[14:17], v[146:149], v[178:181], v[14:17]
	v_mfma_i32_16x16x64_i8 v[10:13], v[154:157], v[178:181], v[10:13]
	v_mfma_i32_16x16x64_i8 v[6:9], v[146:149], v[186:189], v[6:9]
	v_mfma_i32_16x16x64_i8 v[2:5], v[154:157], v[186:189], v[2:5]
	v_mfma_i32_16x16x64_i8 v[30:33], v[150:153], v[166:169], v[30:33]
	v_mfma_i32_16x16x64_i8 v[26:29], v[158:161], v[166:169], v[26:29]
	v_mfma_i32_16x16x64_i8 v[22:25], v[150:153], v[174:177], v[22:25]
	v_mfma_i32_16x16x64_i8 v[18:21], v[158:161], v[174:177], v[18:21]
	v_mfma_i32_16x16x64_i8 v[14:17], v[150:153], v[182:185], v[14:17]
	v_mfma_i32_16x16x64_i8 v[10:13], v[158:161], v[182:185], v[10:13]
	v_mfma_i32_16x16x64_i8 v[6:9], v[150:153], v[190:193], v[6:9]
	v_mfma_i32_16x16x64_i8 v[2:5], v[158:161], v[190:193], v[2:5]
	s_setprio 0
	s_barrier
	s_add_i32 s51, 0, 0x18000
	v_add_u32_e32 v0, s51, v198
	s_add_i32 s52, 0, 0x1c000
	ds_read_b128 v[114:117], v0
	ds_read_b128 v[118:121], v0 offset:1024
	ds_read_b128 v[138:141], v0 offset:2048
	ds_read_b128 v[142:145], v0 offset:3072
	v_add_u32_e32 v0, s52, v198
	ds_read_b128 v[146:149], v0
	ds_read_b128 v[150:153], v0 offset:1024
	ds_read_b128 v[154:157], v0 offset:2048
	ds_read_b128 v[158:161], v0 offset:3072
	s_add_u32 s54, s28, 0x20000
	ds_read_b128 v[162:165], v199 offset:32768
	ds_read_b128 v[166:169], v199 offset:33792
	ds_read_b128 v[170:173], v199 offset:34816
	ds_read_b128 v[174:177], v199 offset:35840
	ds_read_b128 v[178:181], v199 offset:36864
	ds_read_b128 v[182:185], v199 offset:37888
	ds_read_b128 v[186:189], v199 offset:38912
	ds_read_b128 v[190:193], v199 offset:39936
	s_addc_u32 s55, s29, 0
	s_mov_b32 m0, s85
	s_nop 0
	global_load_lds_dwordx4 v194, s[28:29]
	s_mov_b32 m0, s38
	s_nop 0
	global_load_lds_dwordx4 v196, s[28:29]
	s_mov_b32 m0, s39
	s_nop 0
	global_load_lds_dwordx4 v194, s[54:55]
	s_mov_b32 m0, s40
	s_nop 0
	global_load_lds_dwordx4 v196, s[54:55]
	s_waitcnt vmcnt(8)
	s_waitcnt lgkmcnt(0)
	s_barrier
	s_setprio 1
	s_waitcnt lgkmcnt(0)
	v_mfma_i32_16x16x64_i8 v[134:137], v[114:117], v[162:165], v[134:137]
	v_mfma_i32_16x16x64_i8 v[130:133], v[138:141], v[162:165], v[130:133]
	v_mfma_i32_16x16x64_i8 v[126:129], v[114:117], v[170:173], v[126:129]
	v_mfma_i32_16x16x64_i8 v[122:125], v[138:141], v[170:173], v[122:125]
	v_mfma_i32_16x16x64_i8 v[110:113], v[114:117], v[178:181], v[110:113]
	v_mfma_i32_16x16x64_i8 v[106:109], v[138:141], v[178:181], v[106:109]
	v_mfma_i32_16x16x64_i8 v[102:105], v[114:117], v[186:189], v[102:105]
	v_mfma_i32_16x16x64_i8 v[98:101], v[138:141], v[186:189], v[98:101]
	v_mfma_i32_16x16x64_i8 v[134:137], v[118:121], v[166:169], v[134:137]
	v_mfma_i32_16x16x64_i8 v[130:133], v[142:145], v[166:169], v[130:133]
	v_mfma_i32_16x16x64_i8 v[126:129], v[118:121], v[174:177], v[126:129]
	v_mfma_i32_16x16x64_i8 v[122:125], v[142:145], v[174:177], v[122:125]
	v_mfma_i32_16x16x64_i8 v[110:113], v[118:121], v[182:185], v[110:113]
	v_mfma_i32_16x16x64_i8 v[106:109], v[142:145], v[182:185], v[106:109]
	v_mfma_i32_16x16x64_i8 v[102:105], v[118:121], v[190:193], v[102:105]
	v_mfma_i32_16x16x64_i8 v[98:101], v[142:145], v[190:193], v[98:101]
	s_setprio 0
	s_setprio 1
	v_mfma_i32_16x16x64_i8 v[62:65], v[146:149], v[162:165], v[62:65]
	v_mfma_i32_16x16x64_i8 v[58:61], v[154:157], v[162:165], v[58:61]
	v_mfma_i32_16x16x64_i8 v[54:57], v[146:149], v[170:173], v[54:57]
	v_mfma_i32_16x16x64_i8 v[50:53], v[154:157], v[170:173], v[50:53]
	v_mfma_i32_16x16x64_i8 v[46:49], v[146:149], v[178:181], v[46:49]
	v_mfma_i32_16x16x64_i8 v[42:45], v[154:157], v[178:181], v[42:45]
	v_mfma_i32_16x16x64_i8 v[38:41], v[146:149], v[186:189], v[38:41]
	v_mfma_i32_16x16x64_i8 v[34:37], v[154:157], v[186:189], v[34:37]
	v_mfma_i32_16x16x64_i8 v[62:65], v[150:153], v[166:169], v[62:65]
	v_mfma_i32_16x16x64_i8 v[58:61], v[158:161], v[166:169], v[58:61]
	v_mfma_i32_16x16x64_i8 v[54:57], v[150:153], v[174:177], v[54:57]
	v_mfma_i32_16x16x64_i8 v[50:53], v[158:161], v[174:177], v[50:53]
	v_mfma_i32_16x16x64_i8 v[46:49], v[150:153], v[182:185], v[46:49]
	v_mfma_i32_16x16x64_i8 v[42:45], v[158:161], v[182:185], v[42:45]
	v_mfma_i32_16x16x64_i8 v[38:41], v[150:153], v[190:193], v[38:41]
	v_mfma_i32_16x16x64_i8 v[34:37], v[158:161], v[190:193], v[34:37]
	s_setprio 0
	s_barrier
	v_mov_b32_e32 v0, v195
	ds_read_b128 v[162:165], v199 offset:49152
	ds_read_b128 v[166:169], v199 offset:50176
	ds_read_b128 v[170:173], v199 offset:51200
	ds_read_b128 v[174:177], v199 offset:52224
	ds_read_b128 v[178:181], v199 offset:53248
	ds_read_b128 v[182:185], v199 offset:54272
	ds_read_b128 v[186:189], v199 offset:55296
	ds_read_b128 v[190:193], v199 offset:56320
	s_add_i32 s53, s51, s33
	v_lshl_add_u64 v[200:201], s[30:31], 0, v[0:1]
	v_lshl_add_u64 v[200:201], v[200:201], 0, s[90:91]
	s_mov_b32 m0, s53
	v_mov_b32_e32 v0, v197
	s_add_i32 s54, s53, 0x2000
	global_load_lds_dwordx4 v[200:201], off
	s_mov_b32 m0, s54
	v_lshl_add_u64 v[200:201], s[30:31], 0, v[0:1]
	s_add_u32 s30, s30, 0x20080
	v_lshl_add_u64 v[200:201], v[200:201], 0, s[90:91]
	s_addc_u32 s31, s31, 0
	s_add_i32 s55, s52, s33
	global_load_lds_dwordx4 v[200:201], off
	s_mov_b32 m0, s55
	s_add_i32 s56, s55, 0x2000
	global_load_lds_dwordx4 v195, s[30:31]
	s_mov_b32 m0, s56
	s_nop 0
	global_load_lds_dwordx4 v197, s[30:31]
	s_waitcnt vmcnt(6)
	s_waitcnt lgkmcnt(0)
	s_barrier
	s_setprio 1
	s_waitcnt lgkmcnt(0)
	v_mfma_i32_16x16x64_i8 v[94:97], v[114:117], v[162:165], v[94:97]
	v_mfma_i32_16x16x64_i8 v[90:93], v[138:141], v[162:165], v[90:93]
	v_mfma_i32_16x16x64_i8 v[86:89], v[114:117], v[170:173], v[86:89]
	v_mfma_i32_16x16x64_i8 v[82:85], v[138:141], v[170:173], v[82:85]
	v_mfma_i32_16x16x64_i8 v[78:81], v[114:117], v[178:181], v[78:81]
	v_mfma_i32_16x16x64_i8 v[74:77], v[138:141], v[178:181], v[74:77]
	v_mfma_i32_16x16x64_i8 v[70:73], v[114:117], v[186:189], v[70:73]
	v_mfma_i32_16x16x64_i8 v[66:69], v[138:141], v[186:189], v[66:69]
	v_mfma_i32_16x16x64_i8 v[94:97], v[118:121], v[166:169], v[94:97]
	v_mfma_i32_16x16x64_i8 v[90:93], v[142:145], v[166:169], v[90:93]
	v_mfma_i32_16x16x64_i8 v[86:89], v[118:121], v[174:177], v[86:89]
	v_mfma_i32_16x16x64_i8 v[82:85], v[142:145], v[174:177], v[82:85]
	v_mfma_i32_16x16x64_i8 v[78:81], v[118:121], v[182:185], v[78:81]
	v_mfma_i32_16x16x64_i8 v[74:77], v[142:145], v[182:185], v[74:77]
	v_mfma_i32_16x16x64_i8 v[70:73], v[118:121], v[190:193], v[70:73]
	v_mfma_i32_16x16x64_i8 v[66:69], v[142:145], v[190:193], v[66:69]
	s_setprio 0
	s_setprio 1
	v_mfma_i32_16x16x64_i8 v[30:33], v[146:149], v[162:165], v[30:33]
	v_mfma_i32_16x16x64_i8 v[26:29], v[154:157], v[162:165], v[26:29]
	v_mfma_i32_16x16x64_i8 v[22:25], v[146:149], v[170:173], v[22:25]
	v_mfma_i32_16x16x64_i8 v[18:21], v[154:157], v[170:173], v[18:21]
	v_mfma_i32_16x16x64_i8 v[14:17], v[146:149], v[178:181], v[14:17]
	v_mfma_i32_16x16x64_i8 v[10:13], v[154:157], v[178:181], v[10:13]
	v_mfma_i32_16x16x64_i8 v[6:9], v[146:149], v[186:189], v[6:9]
	v_mfma_i32_16x16x64_i8 v[2:5], v[154:157], v[186:189], v[2:5]
	v_mfma_i32_16x16x64_i8 v[30:33], v[150:153], v[166:169], v[30:33]
	v_mfma_i32_16x16x64_i8 v[26:29], v[158:161], v[166:169], v[26:29]
	v_mfma_i32_16x16x64_i8 v[22:25], v[150:153], v[174:177], v[22:25]
	v_mfma_i32_16x16x64_i8 v[18:21], v[158:161], v[174:177], v[18:21]
	v_mfma_i32_16x16x64_i8 v[14:17], v[150:153], v[182:185], v[14:17]
	v_mfma_i32_16x16x64_i8 v[10:13], v[158:161], v[182:185], v[10:13]
	v_mfma_i32_16x16x64_i8 v[6:9], v[150:153], v[190:193], v[6:9]
	v_mfma_i32_16x16x64_i8 v[2:5], v[158:161], v[190:193], v[2:5]
	s_setprio 0
	s_barrier
	v_mov_b32_e32 v0, v194
	s_mov_b32 m0, s41
	v_lshl_add_u64 v[192:193], s[28:29], 0, v[0:1]
	v_lshl_add_u64 v[192:193], v[192:193], 0, s[90:91]
	v_mov_b32_e32 v0, v196
	global_load_lds_dwordx4 v[192:193], off
	s_mov_b32 m0, s42
	v_lshl_add_u64 v[192:193], s[28:29], 0, v[0:1]
	v_lshl_add_u64 v[192:193], v[192:193], 0, s[90:91]
	global_load_lds_dwordx4 v[192:193], off
	s_add_i32 s68, s68, 2
	s_add_u32 s8, s8, 0x100
	s_addc_u32 s9, s9, 0
	s_add_u32 s66, s66, 0x100
	s_addc_u32 s67, s67, 0
	s_cmp_gt_u32 s68, 5
	s_cbranch_scc0 .LBB0_775
	v_readlane_b32 s8, v254, 19
	v_readlane_b32 s9, v254, 20
	s_and_b64 vcc, exec, s[8:9]
	v_mbcnt_lo_u32_b32 v0, -1, 0
	v_mbcnt_hi_u32_b32 v0, -1, v0
	s_or_b32 s30, s63, s72
	v_and_or_b32 v180, v0, 15, s61
	v_or_b32_e32 v178, 16, v180
	v_ashrrev_i32_e32 v179, 31, v178
	v_or_b32_e32 v176, 32, v180
	v_lshl_add_u64 v[114:115], v[178:179], 2, s[20:21]
	v_ashrrev_i32_e32 v177, 31, v176
	v_or_b32_e32 v172, 48, v180
	global_load_dword v150, v[114:115], off
	v_lshl_add_u64 v[114:115], v[176:177], 2, s[20:21]
	v_ashrrev_i32_e32 v173, 31, v172
	v_add_u32_e32 v170, 0x80, v180
	global_load_dword v148, v[114:115], off
	v_lshl_add_u64 v[114:115], v[172:173], 2, s[20:21]
	v_ashrrev_i32_e32 v171, 31, v170
	v_add_u32_e32 v168, 0x90, v180
	global_load_dword v146, v[114:115], off
	v_lshl_add_u64 v[114:115], v[170:171], 2, s[20:21]
	v_ashrrev_i32_e32 v169, 31, v168
	v_add_u32_e32 v164, 0xa0, v180
	v_lshrrev_b32_e32 v0, 1, v0
	global_load_dword v144, v[114:115], off
	v_lshl_add_u64 v[114:115], v[168:169], 2, s[20:21]
	v_ashrrev_i32_e32 v165, 31, v164
	v_add_u32_e32 v160, 0xb0, v180
	v_and_b32_e32 v139, 24, v0
	global_load_dword v142, v[114:115], off
	v_lshl_add_u64 v[114:115], v[164:165], 2, s[20:21]
	v_ashrrev_i32_e32 v161, 31, v160
	v_or_b32_e32 v0, s30, v139
	global_load_dword v140, v[114:115], off
	v_lshl_add_u64 v[114:115], v[160:161], 2, s[20:21]
	v_lshl_add_u64 v[118:119], v[0:1], 2, s[22:23]
	global_load_dword v138, v[114:115], off
	global_load_dwordx4 v[152:155], v[118:119], off offset:16
	global_load_dwordx4 v[182:185], v[118:119], off
	s_nop 0
	global_load_dwordx4 v[114:117], v[118:119], off offset:528
	s_nop 0
	global_load_dwordx4 v[118:121], v[118:119], off offset:512
	s_cbranch_vccz .LBB0_778
	s_barrier
.LBB0_778:
	s_cmpk_lt_u32 s63, 0x200
	s_cselect_b64 vcc, -1, 0
	v_ashrrev_i32_e32 v181, 31, v180
	v_cndmask_b32_e32 v158, 1.0, v243, vcc
	v_cvt_f32_i32_e32 v131, v131
	v_cvt_f32_i32_e32 v130, v130
	v_cvt_f32_i32_e32 v135, v135
	v_cvt_f32_i32_e32 v134, v134
	v_cvt_f32_i32_e32 v137, v137
	v_cvt_f32_i32_e32 v136, v136
	v_cvt_f32_i32_e32 v133, v133
	v_cvt_f32_i32_e32 v132, v132
	v_cvt_f32_i32_e32 v127, v127
	v_cvt_f32_i32_e32 v126, v126
	v_cvt_f32_i32_e32 v129, v129
	v_cvt_f32_i32_e32 v128, v128
	v_cvt_f32_i32_e32 v123, v123
	v_cvt_f32_i32_e32 v122, v122
	v_cvt_f32_i32_e32 v125, v125
	v_cvt_f32_i32_e32 v124, v124
	s_movk_i32 s28, 0x1200
	v_cvt_f32_i32_e32 v111, v111
	v_cvt_f32_i32_e32 v110, v110
	v_cvt_f32_i32_e32 v113, v113
	v_cvt_f32_i32_e32 v112, v112
	v_cvt_f32_i32_e32 v107, v107
	v_cvt_f32_i32_e32 v106, v106
	v_cvt_f32_i32_e32 v109, v109
	v_cvt_f32_i32_e32 v108, v108
	v_cvt_f32_i32_e32 v103, v103
	v_cvt_f32_i32_e32 v102, v102
	v_cvt_f32_i32_e32 v105, v105
	v_cvt_f32_i32_e32 v104, v104
	v_cvt_f32_i32_e32 v99, v99
	v_cvt_f32_i32_e32 v98, v98
	v_cvt_f32_i32_e32 v101, v101
	v_cvt_f32_i32_e32 v100, v100
	v_cvt_f32_i32_e32 v95, v95
	v_cvt_f32_i32_e32 v94, v94
	v_cvt_f32_i32_e32 v97, v97
	v_cvt_f32_i32_e32 v96, v96
	v_cvt_f32_i32_e32 v91, v91
	v_cvt_f32_i32_e32 v90, v90
	v_cvt_f32_i32_e32 v93, v93
	v_cvt_f32_i32_e32 v92, v92
	v_cvt_f32_i32_e32 v87, v87
	v_cvt_f32_i32_e32 v86, v86
	v_cvt_f32_i32_e32 v89, v89
	v_cvt_f32_i32_e32 v88, v88
	v_cvt_f32_i32_e32 v83, v83
	v_cvt_f32_i32_e32 v82, v82
	v_cvt_f32_i32_e32 v85, v85
	v_cvt_f32_i32_e32 v84, v84
	v_cvt_f32_i32_e32 v79, v79
	v_cvt_f32_i32_e32 v78, v78
	v_cvt_f32_i32_e32 v81, v81
	v_cvt_f32_i32_e32 v80, v80
	v_cvt_f32_i32_e32 v75, v75
	v_cvt_f32_i32_e32 v74, v74
	v_cvt_f32_i32_e32 v77, v77
	v_cvt_f32_i32_e32 v76, v76
	v_cvt_f32_i32_e32 v71, v71
	v_cvt_f32_i32_e32 v70, v70
	v_cvt_f32_i32_e32 v73, v73
	v_cvt_f32_i32_e32 v72, v72
	v_cvt_f32_i32_e32 v67, v67
	v_cvt_f32_i32_e32 v66, v66
	v_cvt_f32_i32_e32 v69, v69
	v_cvt_f32_i32_e32 v68, v68
	s_cmpk_eq_i32 s30, 0x800
	s_waitcnt vmcnt(0)
	v_pk_mul_f32 v[188:189], v[158:159], v[154:155] op_sel_hi:[0,1]
	v_lshl_add_u64 v[154:155], v[180:181], 2, s[20:21]
	global_load_dword v166, v[154:155], off
	v_pk_mul_f32 v[152:153], v[158:159], v[152:153] op_sel_hi:[0,1]
	v_pk_mul_f32 v[192:193], v[158:159], v[184:185] op_sel_hi:[0,1]
	v_pk_mul_f32 v[190:191], v[158:159], v[182:183] op_sel_hi:[0,1]
	v_pk_mul_f32 v[130:131], v[152:153], v[130:131]
	v_pk_mul_f32 v[136:137], v[192:193], v[136:137]
	v_pk_mul_f32 v[134:135], v[190:191], v[134:135]
	v_pk_mul_f32 v[132:133], v[188:189], v[132:133]
	v_pk_mul_f32 v[128:129], v[192:193], v[128:129]
	v_pk_mul_f32 v[126:127], v[190:191], v[126:127]
	v_pk_mul_f32 v[124:125], v[188:189], v[124:125]
	v_pk_mul_f32 v[122:123], v[152:153], v[122:123]
	v_pk_mul_f32 v[128:129], v[150:151], v[128:129] op_sel_hi:[0,1]
	v_pk_mul_f32 v[126:127], v[150:151], v[126:127] op_sel_hi:[0,1]
	v_pk_mul_f32 v[112:113], v[192:193], v[112:113]
	v_pk_mul_f32 v[110:111], v[190:191], v[110:111]
	v_pk_mul_f32 v[108:109], v[188:189], v[108:109]
	v_pk_mul_f32 v[106:107], v[152:153], v[106:107]
	v_pk_mul_f32 v[112:113], v[148:149], v[112:113] op_sel_hi:[0,1]
	v_pk_mul_f32 v[110:111], v[148:149], v[110:111] op_sel_hi:[0,1]
	v_pk_mul_f32 v[104:105], v[192:193], v[104:105]
	v_pk_mul_f32 v[102:103], v[190:191], v[102:103]
	v_pk_mul_f32 v[100:101], v[188:189], v[100:101]
	v_pk_mul_f32 v[98:99], v[152:153], v[98:99]
	v_pk_mul_f32 v[104:105], v[146:147], v[104:105] op_sel_hi:[0,1]
	v_pk_mul_f32 v[102:103], v[146:147], v[102:103] op_sel_hi:[0,1]
	v_pk_mul_f32 v[96:97], v[192:193], v[96:97]
	v_pk_mul_f32 v[94:95], v[190:191], v[94:95]
	v_pk_mul_f32 v[92:93], v[188:189], v[92:93]
	v_pk_mul_f32 v[90:91], v[152:153], v[90:91]
	v_pk_mul_f32 v[96:97], v[144:145], v[96:97] op_sel_hi:[0,1]
	v_pk_mul_f32 v[94:95], v[144:145], v[94:95] op_sel_hi:[0,1]
	v_pk_mul_f32 v[88:89], v[192:193], v[88:89]
	v_pk_mul_f32 v[86:87], v[190:191], v[86:87]
	v_pk_mul_f32 v[84:85], v[188:189], v[84:85]
	v_pk_mul_f32 v[82:83], v[152:153], v[82:83]
	v_pk_mul_f32 v[88:89], v[142:143], v[88:89] op_sel_hi:[0,1]
	v_pk_mul_f32 v[86:87], v[142:143], v[86:87] op_sel_hi:[0,1]
	v_pk_mul_f32 v[80:81], v[192:193], v[80:81]
	v_pk_mul_f32 v[78:79], v[190:191], v[78:79]
	v_pk_mul_f32 v[76:77], v[188:189], v[76:77]
	v_pk_mul_f32 v[74:75], v[152:153], v[74:75]
	v_pk_mul_f32 v[80:81], v[140:141], v[80:81] op_sel_hi:[0,1]
	v_pk_mul_f32 v[78:79], v[140:141], v[78:79] op_sel_hi:[0,1]
	v_pk_mul_f32 v[72:73], v[192:193], v[72:73]
	v_pk_mul_f32 v[70:71], v[190:191], v[70:71]
	v_pk_mul_f32 v[68:69], v[188:189], v[68:69]
	v_pk_mul_f32 v[66:67], v[152:153], v[66:67]
	v_pk_mul_f32 v[72:73], v[138:139], v[72:73] op_sel_hi:[0,1]
	v_pk_mul_f32 v[70:71], v[138:139], v[70:71] op_sel_hi:[0,1]
	s_waitcnt vmcnt(0)
	v_pk_mul_f32 v[156:157], v[130:131], v[166:167] op_sel_hi:[1,0]
	v_mov_b64_e32 v[130:131], s[12:13]
	v_pk_mul_f32 v[136:137], v[136:137], v[166:167] op_sel_hi:[1,0]
	v_pk_mul_f32 v[134:135], v[134:135], v[166:167] op_sel_hi:[1,0]
	v_pk_mul_f32 v[154:155], v[132:133], v[166:167] op_sel_hi:[1,0]
	v_mad_i64_i32 v[162:163], s[8:9], v180, s28, v[130:131]
	v_lshlrev_b64 v[132:133], 1, v[0:1]
	v_lshl_add_u64 v[174:175], v[162:163], 0, v[132:133]
	v_cvt_pk_bf16_f32 v134, v134, v135
	v_cvt_pk_bf16_f32 v135, v136, v137
	v_cvt_pk_bf16_f32 v136, v156, v157
	v_cvt_pk_bf16_f32 v137, v154, v155
	global_store_dwordx4 v[174:175], v[134:137], off
	v_mad_i64_i32 v[186:187], s[8:9], v178, s28, v[130:131]
	s_nop 0
	v_pk_mul_f32 v[134:135], v[150:151], v[124:125] op_sel_hi:[0,1]
	v_pk_mul_f32 v[124:125], v[150:151], v[122:123] op_sel_hi:[0,1]
	v_lshl_add_u64 v[136:137], v[186:187], 0, v[132:133]
	v_cvt_pk_bf16_f32 v122, v126, v127
	v_cvt_pk_bf16_f32 v123, v128, v129
	v_cvt_pk_bf16_f32 v124, v124, v125
	v_cvt_pk_bf16_f32 v125, v134, v135
	global_store_dwordx4 v[136:137], v[122:125], off
	v_mad_i64_i32 v[184:185], s[8:9], v176, s28, v[130:131]
	s_nop 0
	v_pk_mul_f32 v[122:123], v[148:149], v[108:109] op_sel_hi:[0,1]
	v_pk_mul_f32 v[108:109], v[148:149], v[106:107] op_sel_hi:[0,1]
	v_lshl_add_u64 v[124:125], v[184:185], 0, v[132:133]
	v_cvt_pk_bf16_f32 v106, v110, v111
	v_cvt_pk_bf16_f32 v107, v112, v113
	v_cvt_pk_bf16_f32 v108, v108, v109
	v_cvt_pk_bf16_f32 v109, v122, v123
	global_store_dwordx4 v[124:125], v[106:109], off
	v_mad_i64_i32 v[182:183], s[8:9], v172, s28, v[130:131]
	s_nop 0
	v_pk_mul_f32 v[106:107], v[146:147], v[100:101] op_sel_hi:[0,1]
	v_pk_mul_f32 v[100:101], v[146:147], v[98:99] op_sel_hi:[0,1]
	v_lshl_add_u64 v[108:109], v[182:183], 0, v[132:133]
	v_cvt_pk_bf16_f32 v98, v102, v103
	v_cvt_pk_bf16_f32 v99, v104, v105
	v_cvt_pk_bf16_f32 v100, v100, v101
	v_cvt_pk_bf16_f32 v101, v106, v107
	global_store_dwordx4 v[108:109], v[98:101], off
	v_mad_i64_i32 v[174:175], s[8:9], v170, s28, v[130:131]
	s_nop 0
	v_pk_mul_f32 v[98:99], v[144:145], v[92:93] op_sel_hi:[0,1]
	v_pk_mul_f32 v[92:93], v[144:145], v[90:91] op_sel_hi:[0,1]
	v_lshl_add_u64 v[100:101], v[174:175], 0, v[132:133]
	v_cvt_pk_bf16_f32 v90, v94, v95
	v_cvt_pk_bf16_f32 v91, v96, v97
	v_cvt_pk_bf16_f32 v92, v92, v93
	v_cvt_pk_bf16_f32 v93, v98, v99
	global_store_dwordx4 v[100:101], v[90:93], off
	v_mad_i64_i32 v[156:157], s[8:9], v168, s28, v[130:131]
	s_nop 0
	v_pk_mul_f32 v[90:91], v[142:143], v[84:85] op_sel_hi:[0,1]
	v_pk_mul_f32 v[84:85], v[142:143], v[82:83] op_sel_hi:[0,1]
	v_lshl_add_u64 v[92:93], v[156:157], 0, v[132:133]
	v_cvt_pk_bf16_f32 v82, v86, v87
	v_cvt_pk_bf16_f32 v83, v88, v89
	v_cvt_pk_bf16_f32 v84, v84, v85
	v_cvt_pk_bf16_f32 v85, v90, v91
	global_store_dwordx4 v[92:93], v[82:85], off
	v_mad_i64_i32 v[154:155], s[8:9], v164, s28, v[130:131]
	s_nop 0
	v_pk_mul_f32 v[82:83], v[140:141], v[76:77] op_sel_hi:[0,1]
	v_pk_mul_f32 v[76:77], v[140:141], v[74:75] op_sel_hi:[0,1]
	v_lshl_add_u64 v[84:85], v[154:155], 0, v[132:133]
	v_cvt_pk_bf16_f32 v74, v78, v79
	v_cvt_pk_bf16_f32 v75, v80, v81
	v_cvt_pk_bf16_f32 v76, v76, v77
	v_cvt_pk_bf16_f32 v77, v82, v83
	global_store_dwordx4 v[84:85], v[74:77], off
	v_mad_i64_i32 v[152:153], s[8:9], v160, s28, v[130:131]
	s_nop 0
	v_pk_mul_f32 v[74:75], v[138:139], v[68:69] op_sel_hi:[0,1]
	v_pk_mul_f32 v[68:69], v[138:139], v[66:67] op_sel_hi:[0,1]
	v_lshl_add_u64 v[76:77], v[152:153], 0, v[132:133]
	v_cvt_pk_bf16_f32 v66, v70, v71
	v_cvt_pk_bf16_f32 v67, v72, v73
	v_cvt_pk_bf16_f32 v68, v68, v69
	v_cvt_pk_bf16_f32 v69, v74, v75
	s_cselect_b64 s[28:29], -1, 0
	s_cmpk_lg_i32 s30, 0x800
	global_store_dwordx4 v[76:77], v[66:69], off
	s_cbranch_scc1 .LBB0_780
	v_lshlrev_b32_e32 v0, 2, v139
	v_lshl_add_u64 v[66:67], s[14:15], 0, v[0:1]
	v_lshlrev_b64 v[68:69], 7, v[180:181]
	v_lshl_add_u64 v[68:69], v[66:67], 0, v[68:69]
	global_load_dwordx4 v[130:133], v[68:69], off offset:16
	global_load_dwordx4 v[134:137], v[68:69], off
	v_lshlrev_b64 v[68:69], 7, v[178:179]
	v_lshl_add_u64 v[68:69], v[66:67], 0, v[68:69]
	global_load_dwordx4 v[122:125], v[68:69], off offset:16
	global_load_dwordx4 v[126:129], v[68:69], off
	v_lshlrev_b64 v[68:69], 7, v[176:177]
	v_lshl_add_u64 v[68:69], v[66:67], 0, v[68:69]
	global_load_dwordx4 v[106:109], v[68:69], off offset:16
	global_load_dwordx4 v[110:113], v[68:69], off
	v_lshlrev_b64 v[68:69], 7, v[172:173]
	v_lshl_add_u64 v[68:69], v[66:67], 0, v[68:69]
	global_load_dwordx4 v[98:101], v[68:69], off offset:16
	global_load_dwordx4 v[102:105], v[68:69], off
	v_lshlrev_b64 v[68:69], 7, v[170:171]
	v_lshl_add_u64 v[68:69], v[66:67], 0, v[68:69]
	global_load_dwordx4 v[90:93], v[68:69], off offset:16
	global_load_dwordx4 v[94:97], v[68:69], off
	v_lshlrev_b64 v[68:69], 7, v[168:169]
	v_lshl_add_u64 v[68:69], v[66:67], 0, v[68:69]
	global_load_dwordx4 v[82:85], v[68:69], off offset:16
	global_load_dwordx4 v[86:89], v[68:69], off
	v_lshlrev_b64 v[68:69], 7, v[164:165]
	v_lshl_add_u64 v[68:69], v[66:67], 0, v[68:69]
	global_load_dwordx4 v[74:77], v[68:69], off offset:16
	global_load_dwordx4 v[78:81], v[68:69], off
	v_lshlrev_b64 v[68:69], 7, v[160:161]
	v_lshl_add_u64 v[70:71], v[66:67], 0, v[68:69]
	global_load_dwordx4 v[66:69], v[70:71], off offset:16
	s_nop 0
	global_load_dwordx4 v[70:73], v[70:71], off

.LBB0_1124:
	s_waitcnt lgkmcnt(7)
	v_rcp_f32_e32 v80, v80
	v_rcp_f32_e32 v81, v81
	s_waitcnt lgkmcnt(6)
	v_rcp_f32_e32 v78, v78
	v_rcp_f32_e32 v79, v79
	s_waitcnt lgkmcnt(5)
	v_rcp_f32_e32 v76, v76
	v_rcp_f32_e32 v77, v77
	s_waitcnt lgkmcnt(4)
	v_rcp_f32_e32 v74, v74
	v_rcp_f32_e32 v75, v75
	s_waitcnt lgkmcnt(3)
	v_rcp_f32_e32 v72, v72
	v_rcp_f32_e32 v73, v73
	s_waitcnt lgkmcnt(2)
	v_rcp_f32_e32 v70, v70
	v_rcp_f32_e32 v71, v71
	s_waitcnt lgkmcnt(1)
	v_rcp_f32_e32 v68, v68
	v_rcp_f32_e32 v69, v69
	s_waitcnt lgkmcnt(0)
	v_rcp_f32_e32 v66, v66
	v_rcp_f32_e32 v67, v67
	s_waitcnt lgkmcnt(0)
	s_barrier
	v_mov_b64_e32 v[82:83], v[130:131]
	s_mov_b64 s[12:13], -1
	s_and_b64 vcc, exec, s[2:3]
	s_cbranch_vccz .LBB0_1126
	global_load_dword v87, v[160:161], off
	global_load_dword v204, v[160:161], off offset:128
	global_load_dword v205, v[160:161], off offset:256
	global_load_dword v206, v[160:161], off offset:384
	global_load_dwordx4 v[82:85], v[132:133], off
	v_readlane_b32 s4, v255, 46
	v_readlane_b32 s5, v255, 47
	global_load_dwordx4 v[92:95], v[136:137], off
	global_load_dwordx4 v[212:215], v[134:135], off
	global_load_dwordx4 v[216:219], v[138:139], off
	global_load_dwordx4 v[228:231], v[140:141], off
	global_load_dwordx4 v[244:247], v[142:143], off
	global_load_dwordx4 v[248:251], v[144:145], off
	global_load_dwordx4 v[88:91], v[146:147], off
	s_waitcnt vmcnt(7)
	v_lshlrev_b32_e32 v207, 16, v82
	v_and_b32_e32 v181, 0xffff0000, v82
	v_lshlrev_b32_e32 v173, 16, v83
	v_and_b32_e32 v165, 0xffff0000, v83
	v_lshlrev_b32_e32 v126, 16, v84
	v_and_b32_e32 v122, 0xffff0000, v84
	v_lshlrev_b32_e32 v117, 16, v85
	v_and_b32_e32 v112, 0xffff0000, v85
	s_waitcnt vmcnt(6)
	v_lshlrev_b32_e32 v208, 16, v92
	v_and_b32_e32 v200, 0xffff0000, v92
	v_lshlrev_b32_e32 v179, 16, v93
	v_and_b32_e32 v171, 0xffff0000, v93
	v_lshlrev_b32_e32 v129, 16, v94
	v_and_b32_e32 v125, 0xffff0000, v94
	v_lshlrev_b32_e32 v120, 16, v95
	v_and_b32_e32 v115, 0xffff0000, v95
	s_waitcnt vmcnt(5)
	v_lshlrev_b32_e32 v110, 16, v212
	v_and_b32_e32 v106, 0xffff0000, v212
	v_lshlrev_b32_e32 v102, 16, v213
	v_and_b32_e32 v98, 0xffff0000, v213
	v_lshlrev_b32_e32 v83, 16, v215
	v_and_b32_e32 v0, 0xffff0000, v215
	v_lshlrev_b32_e32 v94, 16, v214
	v_and_b32_e32 v86, 0xffff0000, v214
	s_waitcnt vmcnt(4)
	v_lshlrev_b32_e32 v114, 16, v216
	v_and_b32_e32 v109, 0xffff0000, v216
	v_lshlrev_b32_e32 v105, 16, v217
	v_and_b32_e32 v101, 0xffff0000, v217
	v_lshlrev_b32_e32 v97, 16, v218
	v_and_b32_e32 v93, 0xffff0000, v218
	v_lshlrev_b32_e32 v85, 16, v219
	v_and_b32_e32 v82, 0xffff0000, v219
	s_waitcnt vmcnt(3)
	v_lshlrev_b32_e32 v209, 16, v228
	v_and_b32_e32 v202, 0xffff0000, v228
	v_lshlrev_b32_e32 v183, 16, v229
	v_and_b32_e32 v177, 0xffff0000, v229
	v_lshlrev_b32_e32 v169, 16, v230
	v_and_b32_e32 v128, 0xffff0000, v230
	v_lshlrev_b32_e32 v124, 16, v231
	v_and_b32_e32 v119, 0xffff0000, v231
	s_waitcnt vmcnt(2)
	v_lshlrev_b32_e32 v118, 16, v244
	v_and_b32_e32 v113, 0xffff0000, v244
	v_lshlrev_b32_e32 v108, 16, v245
	v_and_b32_e32 v104, 0xffff0000, v245
	v_lshlrev_b32_e32 v100, 16, v246
	v_and_b32_e32 v96, 0xffff0000, v246
	v_lshlrev_b32_e32 v92, 16, v247
	v_and_b32_e32 v84, 0xffff0000, v247
	s_waitcnt vmcnt(1)
	v_lshlrev_b32_e32 v210, 16, v248
	v_and_b32_e32 v203, 0xffff0000, v248
	v_lshlrev_b32_e32 v201, 16, v249
	v_and_b32_e32 v182, 0xffff0000, v249
	v_lshlrev_b32_e32 v175, 16, v250
	v_and_b32_e32 v167, 0xffff0000, v250
	v_lshlrev_b32_e32 v127, 16, v251
	v_and_b32_e32 v123, 0xffff0000, v251
	s_waitcnt vmcnt(0)
	v_lshlrev_b32_e32 v121, 16, v88
	v_and_b32_e32 v116, 0xffff0000, v88
	v_lshlrev_b32_e32 v111, 16, v89
	v_and_b32_e32 v107, 0xffff0000, v89
	v_mul_f32_e32 v89, v185, v204
	v_mul_f32_e32 v88, v185, v205
	v_mov_b64_e32 v[204:205], v[162:163]
	v_lshlrev_b32_e32 v103, 16, v90
	v_and_b32_e32 v99, 0xffff0000, v90
	v_mul_f32_e32 v90, v185, v87
	v_mul_f32_e32 v87, v185, v206
	v_lshlrev_b32_e32 v95, 16, v91
	v_and_b32_e32 v91, 0xffff0000, v91
	s_nop 0
	v_mul_f32_e32 v205, v34, v80
	v_mul_f32_e32 v204, v50, v80
	v_fma_f32 v205, -v184, v205, v208
	v_fma_f32 v204, -v184, v204, v207
	v_mul_f32_e32 v207, v18, v80
	v_mul_f32_e32 v208, v2, v80
	v_mul_f32_e32 v206, v205, v205
	v_fma_f32 v207, -v184, v207, v209
	v_fma_f32 v208, -v184, v208, v210
	v_fmac_f32_e32 v206, v204, v204
	v_fmac_f32_e32 v206, v207, v207
	v_fmac_f32_e32 v206, v208, v208
	s_nop 1
	v_add_f32_dpp v206, v206, v206 quad_perm:[1,0,3,2] row_mask:0xf bank_mask:0xf bound_ctrl:1
	s_nop 1
	v_add_f32_dpp v206, v206, v206 quad_perm:[2,3,0,1] row_mask:0xf bank_mask:0xf bound_ctrl:1
	s_nop 1
	v_add_f32_dpp v206, v206, v206 row_ror:4 row_mask:0xf bank_mask:0xf bound_ctrl:1
	s_nop 1
	v_add_f32_dpp v206, v206, v206 row_ror:8 row_mask:0xf bank_mask:0xf bound_ctrl:1
	ds_swizzle_b32 v209, v206 offset:swizzle(SWAP,16)
	s_waitcnt lgkmcnt(0)
	v_add_f32_e32 v206, v206, v209
	v_fmamk_f32 v206, v206, 0x3c000000, v232
	v_rsq_f32_e32 v206, v206
	s_nop 0
	v_mul_f32_e32 v204, v204, v206
	v_mul_f32_e32 v204, v90, v204
	v_cvt_pk_bf16_f32 v204, v204, s0
	ds_write_b16 v193, v204
	v_mul_f32_e32 v204, v205, v206
	v_mul_f32_e32 v205, v19, v81
	v_mul_f32_e32 v204, v89, v204
	v_fma_f32 v202, -v184, v205, v202
	v_mul_f32_e32 v205, v3, v81
	v_cvt_pk_bf16_f32 v204, v204, s0
	ds_write_b16 v193, v204 offset:64
	v_mul_f32_e32 v204, v207, v206
	v_mul_f32_e32 v204, v88, v204
	v_cvt_pk_bf16_f32 v204, v204, s0
	ds_write_b16 v193, v204 offset:128
	v_mul_f32_e32 v204, v208, v206
	v_mul_f32_e32 v204, v87, v204
	v_cvt_pk_bf16_f32 v204, v204, s0
	ds_write_b16 v193, v204 offset:192
	v_mul_f32_e32 v204, v51, v81
	v_fma_f32 v181, -v184, v204, v181
	v_mul_f32_e32 v204, v35, v81
	v_fma_f32 v200, -v184, v204, v200
	v_mul_f32_e32 v204, v200, v200
	v_fmac_f32_e32 v204, v181, v181
	v_fmac_f32_e32 v204, v202, v202
	v_fma_f32 v203, -v184, v205, v203
	v_fmac_f32_e32 v204, v203, v203
	s_nop 1
	v_add_f32_dpp v204, v204, v204 quad_perm:[1,0,3,2] row_mask:0xf bank_mask:0xf bound_ctrl:1
	s_nop 1
	v_add_f32_dpp v204, v204, v204 quad_perm:[2,3,0,1] row_mask:0xf bank_mask:0xf bound_ctrl:1
	s_nop 1
	v_add_f32_dpp v204, v204, v204 row_ror:4 row_mask:0xf bank_mask:0xf bound_ctrl:1
	s_nop 1
	v_add_f32_dpp v204, v204, v204 row_ror:8 row_mask:0xf bank_mask:0xf bound_ctrl:1
	ds_swizzle_b32 v205, v204 offset:swizzle(SWAP,16)
	s_waitcnt lgkmcnt(0)
	v_add_f32_e32 v204, v204, v205
	v_fmamk_f32 v204, v204, 0x3c000000, v232
	v_rsq_f32_e32 v204, v204
	s_nop 0
	v_mul_f32_e32 v181, v181, v204
	v_mul_f32_e32 v181, v90, v181
	v_cvt_pk_bf16_f32 v181, v181, s0
	ds_write_b16 v193, v181 offset:272
	v_mul_f32_e32 v181, v200, v204
	v_mul_f32_e32 v181, v89, v181
	v_cvt_pk_bf16_f32 v181, v181, s0
	ds_write_b16 v193, v181 offset:336
	v_mul_f32_e32 v181, v202, v204
	v_mul_f32_e32 v181, v88, v181
	v_cvt_pk_bf16_f32 v181, v181, s0
	ds_write_b16 v193, v181 offset:400
	v_mul_f32_e32 v181, v203, v204
	v_mul_f32_e32 v181, v87, v181
	v_cvt_pk_bf16_f32 v181, v181, s0
	ds_write_b16 v193, v181 offset:464
	v_mul_f32_e32 v181, v52, v78
	v_fma_f32 v173, -v184, v181, v173
	v_mul_f32_e32 v181, v36, v78
	v_fma_f32 v179, -v184, v181, v179
	v_mul_f32_e32 v181, v179, v179
	v_mul_f32_e32 v200, v20, v78
	v_fmac_f32_e32 v181, v173, v173
	v_fma_f32 v183, -v184, v200, v183
	v_mul_f32_e32 v200, v4, v78
	v_fmac_f32_e32 v181, v183, v183
	v_fma_f32 v200, -v184, v200, v201
	v_fmac_f32_e32 v181, v200, v200
	s_nop 1
	v_add_f32_dpp v181, v181, v181 quad_perm:[1,0,3,2] row_mask:0xf bank_mask:0xf bound_ctrl:1
	s_nop 1
	v_add_f32_dpp v181, v181, v181 quad_perm:[2,3,0,1] row_mask:0xf bank_mask:0xf bound_ctrl:1
	s_nop 1
	v_add_f32_dpp v181, v181, v181 row_ror:4 row_mask:0xf bank_mask:0xf bound_ctrl:1
	s_nop 1
	v_add_f32_dpp v181, v181, v181 row_ror:8 row_mask:0xf bank_mask:0xf bound_ctrl:1
	ds_swizzle_b32 v201, v181 offset:swizzle(SWAP,16)
	s_waitcnt lgkmcnt(0)
	v_add_f32_e32 v181, v181, v201
	v_fmamk_f32 v181, v181, 0x3c000000, v232
	v_rsq_f32_e32 v181, v181
	s_nop 0
	v_mul_f32_e32 v173, v173, v181
	v_mul_f32_e32 v173, v90, v173
	v_cvt_pk_bf16_f32 v173, v173, s0
	ds_write_b16 v193, v173 offset:544
	v_mul_f32_e32 v173, v179, v181
	v_mul_f32_e32 v173, v89, v173
	v_cvt_pk_bf16_f32 v173, v173, s0
	ds_write_b16 v193, v173 offset:608
	v_mul_f32_e32 v173, v183, v181
	v_mul_f32_e32 v173, v88, v173
	v_cvt_pk_bf16_f32 v173, v173, s0
	ds_write_b16 v193, v173 offset:672
	v_mul_f32_e32 v173, v200, v181
	v_mul_f32_e32 v173, v87, v173
	v_cvt_pk_bf16_f32 v173, v173, s0
	ds_write_b16 v193, v173 offset:736
	v_mul_f32_e32 v173, v53, v79
	v_fma_f32 v165, -v184, v173, v165
	v_mul_f32_e32 v173, v37, v79
	v_fma_f32 v171, -v184, v173, v171
	v_mul_f32_e32 v173, v171, v171
	v_mul_f32_e32 v179, v21, v79
	v_fmac_f32_e32 v173, v165, v165
	v_fma_f32 v177, -v184, v179, v177
	v_mul_f32_e32 v179, v5, v79
	v_fmac_f32_e32 v173, v177, v177
	v_fma_f32 v179, -v184, v179, v182
	v_fmac_f32_e32 v173, v179, v179
	s_nop 1
	v_add_f32_dpp v173, v173, v173 quad_perm:[1,0,3,2] row_mask:0xf bank_mask:0xf bound_ctrl:1
	s_nop 1
	v_add_f32_dpp v173, v173, v173 quad_perm:[2,3,0,1] row_mask:0xf bank_mask:0xf bound_ctrl:1
	s_nop 1
	v_add_f32_dpp v173, v173, v173 row_ror:4 row_mask:0xf bank_mask:0xf bound_ctrl:1
	s_nop 1
	v_add_f32_dpp v173, v173, v173 row_ror:8 row_mask:0xf bank_mask:0xf bound_ctrl:1
	ds_swizzle_b32 v181, v173 offset:swizzle(SWAP,16)
	s_waitcnt lgkmcnt(0)
	v_add_f32_e32 v173, v173, v181
	v_fmamk_f32 v173, v173, 0x3c000000, v232
	v_rsq_f32_e32 v173, v173
	v_mov_b32_e32 v181, v1
	v_mul_f32_e32 v165, v165, v173
	v_mul_f32_e32 v165, v90, v165
	v_cvt_pk_bf16_f32 v165, v165, s0
	ds_write_b16 v193, v165 offset:816
	v_mul_f32_e32 v165, v171, v173
	v_mul_f32_e32 v165, v89, v165
	v_cvt_pk_bf16_f32 v165, v165, s0
	ds_write_b16 v193, v165 offset:880
	v_mul_f32_e32 v165, v177, v173
	v_mul_f32_e32 v165, v88, v165
	v_cvt_pk_bf16_f32 v165, v165, s0
	ds_write_b16 v193, v165 offset:944
	v_mul_f32_e32 v165, v179, v173
	v_mul_f32_e32 v165, v87, v165
	v_cvt_pk_bf16_f32 v165, v165, s0
	ds_write_b16 v193, v165 offset:1008
	v_mul_f32_e32 v165, v54, v76
	v_fma_f32 v126, -v184, v165, v126
	v_mul_f32_e32 v165, v38, v76
	v_fma_f32 v129, -v184, v165, v129
	v_mul_f32_e32 v165, v129, v129
	v_mul_f32_e32 v171, v22, v76
	v_fmac_f32_e32 v165, v126, v126
	v_fma_f32 v169, -v184, v171, v169
	v_mul_f32_e32 v171, v6, v76
	v_fmac_f32_e32 v165, v169, v169
	v_fma_f32 v171, -v184, v171, v175
	v_fmac_f32_e32 v165, v171, v171
	v_mov_b32_e32 v175, v1
	v_mov_b32_e32 v177, v1
	v_add_f32_dpp v165, v165, v165 quad_perm:[1,0,3,2] row_mask:0xf bank_mask:0xf bound_ctrl:1
	v_mov_b32_e32 v179, v1
	s_nop 0
	v_add_f32_dpp v165, v165, v165 quad_perm:[2,3,0,1] row_mask:0xf bank_mask:0xf bound_ctrl:1
	s_nop 1
	v_add_f32_dpp v165, v165, v165 row_ror:4 row_mask:0xf bank_mask:0xf bound_ctrl:1
	s_nop 1
	v_add_f32_dpp v165, v165, v165 row_ror:8 row_mask:0xf bank_mask:0xf bound_ctrl:1
	ds_swizzle_b32 v173, v165 offset:swizzle(SWAP,16)
	s_waitcnt lgkmcnt(0)
	v_add_f32_e32 v165, v165, v173
	v_fmamk_f32 v165, v165, 0x3c000000, v232
	v_rsq_f32_e32 v165, v165
	v_mov_b32_e32 v173, v1
	v_mul_f32_e32 v126, v126, v165
	v_mul_f32_e32 v126, v90, v126
	v_cvt_pk_bf16_f32 v126, v126, s0
	ds_write_b16 v193, v126 offset:2176
	v_mul_f32_e32 v126, v129, v165
	v_mul_f32_e32 v126, v89, v126
	v_cvt_pk_bf16_f32 v126, v126, s0
	ds_write_b16 v193, v126 offset:2240
	v_mul_f32_e32 v126, v169, v165
	v_mul_f32_e32 v126, v88, v126
	v_cvt_pk_bf16_f32 v126, v126, s0
	ds_write_b16 v193, v126 offset:2304
	v_mul_f32_e32 v126, v171, v165
	v_mul_f32_e32 v126, v87, v126
	v_cvt_pk_bf16_f32 v126, v126, s0
	ds_write_b16 v193, v126 offset:2368
	v_mul_f32_e32 v126, v55, v77
	v_fma_f32 v122, -v184, v126, v122
	v_mul_f32_e32 v126, v39, v77
	v_fma_f32 v125, -v184, v126, v125
	v_mul_f32_e32 v126, v125, v125
	v_mul_f32_e32 v129, v23, v77
	v_fmac_f32_e32 v126, v122, v122
	v_fma_f32 v128, -v184, v129, v128
	v_mul_f32_e32 v129, v7, v77
	v_fmac_f32_e32 v126, v128, v128
	v_fma_f32 v129, -v184, v129, v167
	v_fmac_f32_e32 v126, v129, v129
	v_mov_b32_e32 v167, v1
	v_mov_b32_e32 v169, v1
	v_add_f32_dpp v126, v126, v126 quad_perm:[1,0,3,2] row_mask:0xf bank_mask:0xf bound_ctrl:1
	v_mov_b32_e32 v171, v1
	s_nop 0
	v_add_f32_dpp v126, v126, v126 quad_perm:[2,3,0,1] row_mask:0xf bank_mask:0xf bound_ctrl:1
	s_nop 1
	v_add_f32_dpp v126, v126, v126 row_ror:4 row_mask:0xf bank_mask:0xf bound_ctrl:1
	s_nop 1
	v_add_f32_dpp v126, v126, v126 row_ror:8 row_mask:0xf bank_mask:0xf bound_ctrl:1
	ds_swizzle_b32 v165, v126 offset:swizzle(SWAP,16)
	s_waitcnt lgkmcnt(0)
	v_add_f32_e32 v126, v126, v165
	v_fmamk_f32 v126, v126, 0x3c000000, v232
	v_rsq_f32_e32 v126, v126
	v_mov_b32_e32 v165, v1
	v_mul_f32_e32 v122, v122, v126
	v_mul_f32_e32 v122, v90, v122
	v_cvt_pk_bf16_f32 v122, v122, s0
	ds_write_b16 v193, v122 offset:2448
	v_mul_f32_e32 v122, v125, v126
	v_mul_f32_e32 v122, v89, v122
	v_cvt_pk_bf16_f32 v122, v122, s0
	ds_write_b16 v193, v122 offset:2512
	v_mul_f32_e32 v122, v128, v126
	v_mul_f32_e32 v122, v88, v122
	v_cvt_pk_bf16_f32 v122, v122, s0
	ds_write_b16 v193, v122 offset:2576
	v_mul_f32_e32 v122, v129, v126
	v_mul_f32_e32 v122, v87, v122
	v_cvt_pk_bf16_f32 v122, v122, s0
	ds_write_b16 v193, v122 offset:2640
	v_mul_f32_e32 v122, v56, v74
	v_fma_f32 v117, -v184, v122, v117
	v_mul_f32_e32 v122, v40, v74
	v_fma_f32 v120, -v184, v122, v120
	v_mul_f32_e32 v122, v120, v120
	v_mul_f32_e32 v125, v24, v74
	v_fmac_f32_e32 v122, v117, v117
	v_fma_f32 v124, -v184, v125, v124
	v_mul_f32_e32 v125, v8, v74
	v_fmac_f32_e32 v122, v124, v124
	v_fma_f32 v125, -v184, v125, v127
	v_fmac_f32_e32 v122, v125, v125
	s_nop 1
	v_add_f32_dpp v122, v122, v122 quad_perm:[1,0,3,2] row_mask:0xf bank_mask:0xf bound_ctrl:1
	s_nop 1
	v_add_f32_dpp v122, v122, v122 quad_perm:[2,3,0,1] row_mask:0xf bank_mask:0xf bound_ctrl:1
	s_nop 1
	v_add_f32_dpp v122, v122, v122 row_ror:4 row_mask:0xf bank_mask:0xf bound_ctrl:1
	s_nop 1
	v_add_f32_dpp v122, v122, v122 row_ror:8 row_mask:0xf bank_mask:0xf bound_ctrl:1
	ds_swizzle_b32 v126, v122 offset:swizzle(SWAP,16)
	s_waitcnt lgkmcnt(0)
	v_add_f32_e32 v122, v122, v126
	v_fmamk_f32 v122, v122, 0x3c000000, v232
	v_rsq_f32_e32 v122, v122
	s_nop 0
	v_mul_f32_e32 v117, v117, v122
	v_mul_f32_e32 v117, v90, v117
	v_cvt_pk_bf16_f32 v117, v117, s0
	ds_write_b16 v193, v117 offset:2720
	v_mul_f32_e32 v117, v120, v122
	v_mul_f32_e32 v117, v89, v117
	v_cvt_pk_bf16_f32 v117, v117, s0
	ds_write_b16 v193, v117 offset:2784
	v_mul_f32_e32 v117, v124, v122
	v_mul_f32_e32 v117, v88, v117
	v_cvt_pk_bf16_f32 v117, v117, s0
	ds_write_b16 v193, v117 offset:2848
	v_mul_f32_e32 v117, v125, v122
	v_mul_f32_e32 v117, v87, v117
	v_cvt_pk_bf16_f32 v117, v117, s0
	ds_write_b16 v193, v117 offset:2912
	v_mul_f32_e32 v117, v57, v75
	v_fma_f32 v112, -v184, v117, v112
	v_mul_f32_e32 v117, v41, v75
	v_fma_f32 v115, -v184, v117, v115
	v_mul_f32_e32 v117, v115, v115
	v_mul_f32_e32 v120, v25, v75
	v_fmac_f32_e32 v117, v112, v112
	v_fma_f32 v119, -v184, v120, v119
	v_mul_f32_e32 v120, v9, v75
	v_fmac_f32_e32 v117, v119, v119
	v_fma_f32 v120, -v184, v120, v123
	v_fmac_f32_e32 v117, v120, v120
	s_nop 1
	v_add_f32_dpp v117, v117, v117 quad_perm:[1,0,3,2] row_mask:0xf bank_mask:0xf bound_ctrl:1
	s_nop 1
	v_add_f32_dpp v117, v117, v117 quad_perm:[2,3,0,1] row_mask:0xf bank_mask:0xf bound_ctrl:1
	s_nop 1
	v_add_f32_dpp v117, v117, v117 row_ror:4 row_mask:0xf bank_mask:0xf bound_ctrl:1
	s_nop 1
	v_add_f32_dpp v117, v117, v117 row_ror:8 row_mask:0xf bank_mask:0xf bound_ctrl:1
	ds_swizzle_b32 v122, v117 offset:swizzle(SWAP,16)
	s_waitcnt lgkmcnt(0)
	v_add_f32_e32 v117, v117, v122
	v_fmamk_f32 v117, v117, 0x3c000000, v232
	v_rsq_f32_e32 v117, v117
	s_nop 0
	v_mul_f32_e32 v112, v112, v117
	v_mul_f32_e32 v112, v90, v112
	v_cvt_pk_bf16_f32 v112, v112, s0
	ds_write_b16 v193, v112 offset:2992
	v_mul_f32_e32 v112, v115, v117
	v_mul_f32_e32 v112, v89, v112
	v_cvt_pk_bf16_f32 v112, v112, s0
	ds_write_b16 v193, v112 offset:3056
	v_mul_f32_e32 v112, v119, v117
	v_mul_f32_e32 v112, v88, v112
	v_cvt_pk_bf16_f32 v112, v112, s0
	ds_write_b16 v193, v112 offset:3120
	v_mul_f32_e32 v112, v120, v117
	v_mul_f32_e32 v112, v87, v112
	v_cvt_pk_bf16_f32 v112, v112, s0
	ds_write_b16 v193, v112 offset:3184
	v_mul_f32_e32 v112, v58, v72
	v_fma_f32 v110, -v184, v112, v110
	v_mul_f32_e32 v112, v42, v72
	v_fma_f32 v112, -v184, v112, v114
	v_mul_f32_e32 v114, v112, v112
	v_mul_f32_e32 v115, v26, v72
	v_fmac_f32_e32 v114, v110, v110
	v_fma_f32 v115, -v184, v115, v118
	v_mul_f32_e32 v117, v10, v72
	v_fmac_f32_e32 v114, v115, v115
	v_fma_f32 v117, -v184, v117, v121
	v_fmac_f32_e32 v114, v117, v117
	s_nop 1
	v_add_f32_dpp v114, v114, v114 quad_perm:[1,0,3,2] row_mask:0xf bank_mask:0xf bound_ctrl:1
	s_nop 1
	v_add_f32_dpp v114, v114, v114 quad_perm:[2,3,0,1] row_mask:0xf bank_mask:0xf bound_ctrl:1
	s_nop 1
	v_add_f32_dpp v114, v114, v114 row_ror:4 row_mask:0xf bank_mask:0xf bound_ctrl:1
	s_nop 1
	v_add_f32_dpp v114, v114, v114 row_ror:8 row_mask:0xf bank_mask:0xf bound_ctrl:1
	ds_swizzle_b32 v118, v114 offset:swizzle(SWAP,16)
	s_waitcnt lgkmcnt(0)
	v_add_f32_e32 v114, v114, v118
	v_fmamk_f32 v114, v114, 0x3c000000, v232
	v_rsq_f32_e32 v114, v114
	s_nop 0
	v_mul_f32_e32 v110, v110, v114
	v_mul_f32_e32 v110, v90, v110
	v_cvt_pk_bf16_f32 v110, v110, s0
	ds_write_b16 v193, v110 offset:4352
	v_mul_f32_e32 v110, v112, v114
	v_mul_f32_e32 v110, v89, v110
	v_cvt_pk_bf16_f32 v110, v110, s0
	ds_write_b16 v193, v110 offset:4416
	v_mul_f32_e32 v110, v115, v114
	v_mul_f32_e32 v110, v88, v110
	v_cvt_pk_bf16_f32 v110, v110, s0
	ds_write_b16 v193, v110 offset:4480
	v_mul_f32_e32 v110, v117, v114
	v_mul_f32_e32 v110, v87, v110
	v_cvt_pk_bf16_f32 v110, v110, s0
	ds_write_b16 v193, v110 offset:4544
	v_mul_f32_e32 v110, v59, v73
	v_fma_f32 v106, -v184, v110, v106
	v_mul_f32_e32 v110, v43, v73
	v_fma_f32 v109, -v184, v110, v109
	v_mul_f32_e32 v110, v109, v109
	v_mul_f32_e32 v112, v27, v73
	v_fmac_f32_e32 v110, v106, v106
	v_fma_f32 v112, -v184, v112, v113
	v_mul_f32_e32 v113, v11, v73
	v_fmac_f32_e32 v110, v112, v112
	v_fma_f32 v113, -v184, v113, v116
	v_fmac_f32_e32 v110, v113, v113
	s_nop 1
	v_add_f32_dpp v110, v110, v110 quad_perm:[1,0,3,2] row_mask:0xf bank_mask:0xf bound_ctrl:1
	s_nop 1
	v_add_f32_dpp v110, v110, v110 quad_perm:[2,3,0,1] row_mask:0xf bank_mask:0xf bound_ctrl:1
	s_nop 1
	v_add_f32_dpp v110, v110, v110 row_ror:4 row_mask:0xf bank_mask:0xf bound_ctrl:1
	s_nop 1
	v_add_f32_dpp v110, v110, v110 row_ror:8 row_mask:0xf bank_mask:0xf bound_ctrl:1
	ds_swizzle_b32 v114, v110 offset:swizzle(SWAP,16)
	s_waitcnt lgkmcnt(0)
	v_add_f32_e32 v110, v110, v114
	v_fmamk_f32 v110, v110, 0x3c000000, v232
	v_rsq_f32_e32 v110, v110
	s_nop 0
	v_mul_f32_e32 v106, v106, v110
	v_mul_f32_e32 v106, v90, v106
	v_cvt_pk_bf16_f32 v106, v106, s0
	ds_write_b16 v193, v106 offset:4624
	v_mul_f32_e32 v106, v109, v110
	v_mul_f32_e32 v106, v89, v106
	v_cvt_pk_bf16_f32 v106, v106, s0
	ds_write_b16 v193, v106 offset:4688
	v_mul_f32_e32 v106, v112, v110
	v_mul_f32_e32 v106, v88, v106
	v_cvt_pk_bf16_f32 v106, v106, s0
	ds_write_b16 v193, v106 offset:4752
	v_mul_f32_e32 v106, v113, v110
	v_mul_f32_e32 v106, v87, v106
	v_cvt_pk_bf16_f32 v106, v106, s0
	ds_write_b16 v193, v106 offset:4816
	v_mul_f32_e32 v106, v60, v70
	v_fma_f32 v102, -v184, v106, v102
	v_mul_f32_e32 v106, v44, v70
	v_fma_f32 v105, -v184, v106, v105
	v_mul_f32_e32 v106, v105, v105
	v_mul_f32_e32 v109, v28, v70
	v_fmac_f32_e32 v106, v102, v102
	v_fma_f32 v108, -v184, v109, v108
	v_mul_f32_e32 v109, v12, v70
	v_fmac_f32_e32 v106, v108, v108
	v_fma_f32 v109, -v184, v109, v111
	v_fmac_f32_e32 v106, v109, v109
	s_nop 1
	v_add_f32_dpp v106, v106, v106 quad_perm:[1,0,3,2] row_mask:0xf bank_mask:0xf bound_ctrl:1
	s_nop 1
	v_add_f32_dpp v106, v106, v106 quad_perm:[2,3,0,1] row_mask:0xf bank_mask:0xf bound_ctrl:1
	s_nop 1
	v_add_f32_dpp v106, v106, v106 row_ror:4 row_mask:0xf bank_mask:0xf bound_ctrl:1
	s_nop 1
	v_add_f32_dpp v106, v106, v106 row_ror:8 row_mask:0xf bank_mask:0xf bound_ctrl:1
	ds_swizzle_b32 v110, v106 offset:swizzle(SWAP,16)
	s_waitcnt lgkmcnt(0)
	v_add_f32_e32 v106, v106, v110
	v_fmamk_f32 v106, v106, 0x3c000000, v232
	v_rsq_f32_e32 v106, v106
	s_nop 0
	v_mul_f32_e32 v102, v102, v106
	v_mul_f32_e32 v102, v90, v102
	v_cvt_pk_bf16_f32 v102, v102, s0
	ds_write_b16 v193, v102 offset:4896
	v_mul_f32_e32 v102, v105, v106
	v_mul_f32_e32 v102, v89, v102
	v_cvt_pk_bf16_f32 v102, v102, s0
	ds_write_b16 v193, v102 offset:4960
	v_mul_f32_e32 v102, v108, v106
	v_mul_f32_e32 v102, v88, v102
	v_cvt_pk_bf16_f32 v102, v102, s0
	ds_write_b16 v193, v102 offset:5024
	v_mul_f32_e32 v102, v109, v106
	v_mul_f32_e32 v102, v87, v102
	v_cvt_pk_bf16_f32 v102, v102, s0
	ds_write_b16 v193, v102 offset:5088
	v_mul_f32_e32 v102, v61, v71
	v_fma_f32 v98, -v184, v102, v98
	v_mul_f32_e32 v102, v45, v71
	v_fma_f32 v101, -v184, v102, v101
	v_mul_f32_e32 v102, v101, v101
	v_mul_f32_e32 v105, v29, v71
	v_fmac_f32_e32 v102, v98, v98
	v_fma_f32 v104, -v184, v105, v104
	v_mul_f32_e32 v105, v13, v71
	v_fmac_f32_e32 v102, v104, v104
	v_fma_f32 v105, -v184, v105, v107
	v_fmac_f32_e32 v102, v105, v105
	s_nop 1
	v_add_f32_dpp v102, v102, v102 quad_perm:[1,0,3,2] row_mask:0xf bank_mask:0xf bound_ctrl:1
	s_nop 1
	v_add_f32_dpp v102, v102, v102 quad_perm:[2,3,0,1] row_mask:0xf bank_mask:0xf bound_ctrl:1
	s_nop 1
	v_add_f32_dpp v102, v102, v102 row_ror:4 row_mask:0xf bank_mask:0xf bound_ctrl:1
	s_nop 1
	v_add_f32_dpp v102, v102, v102 row_ror:8 row_mask:0xf bank_mask:0xf bound_ctrl:1
	ds_swizzle_b32 v106, v102 offset:swizzle(SWAP,16)
	s_waitcnt lgkmcnt(0)
	v_add_f32_e32 v102, v102, v106
	v_fmamk_f32 v102, v102, 0x3c000000, v232
	v_rsq_f32_e32 v102, v102
	s_nop 0
	v_mul_f32_e32 v98, v98, v102
	v_mul_f32_e32 v98, v90, v98
	v_cvt_pk_bf16_f32 v98, v98, s0
	ds_write_b16 v193, v98 offset:5168
	v_mul_f32_e32 v98, v101, v102
	v_mul_f32_e32 v98, v89, v98
	v_cvt_pk_bf16_f32 v98, v98, s0
	ds_write_b16 v193, v98 offset:5232
	v_mul_f32_e32 v98, v104, v102
	v_mul_f32_e32 v98, v88, v98
	v_cvt_pk_bf16_f32 v98, v98, s0
	ds_write_b16 v193, v98 offset:5296
	v_mul_f32_e32 v98, v105, v102
	v_mul_f32_e32 v98, v87, v98
	v_cvt_pk_bf16_f32 v98, v98, s0
	ds_write_b16 v193, v98 offset:5360
	v_mul_f32_e32 v98, v62, v68
	v_fma_f32 v94, -v184, v98, v94
	v_mul_f32_e32 v98, v46, v68
	v_fma_f32 v97, -v184, v98, v97
	v_mul_f32_e32 v98, v97, v97
	v_mul_f32_e32 v101, v30, v68
	v_fmac_f32_e32 v98, v94, v94
	v_fma_f32 v100, -v184, v101, v100
	v_mul_f32_e32 v101, v14, v68
	v_fmac_f32_e32 v98, v100, v100
	v_fma_f32 v101, -v184, v101, v103
	v_fmac_f32_e32 v98, v101, v101
	s_nop 1
	v_add_f32_dpp v98, v98, v98 quad_perm:[1,0,3,2] row_mask:0xf bank_mask:0xf bound_ctrl:1
	s_nop 1
	v_add_f32_dpp v98, v98, v98 quad_perm:[2,3,0,1] row_mask:0xf bank_mask:0xf bound_ctrl:1
	s_nop 1
	v_add_f32_dpp v98, v98, v98 row_ror:4 row_mask:0xf bank_mask:0xf bound_ctrl:1
	s_nop 1
	v_add_f32_dpp v98, v98, v98 row_ror:8 row_mask:0xf bank_mask:0xf bound_ctrl:1
	ds_swizzle_b32 v102, v98 offset:swizzle(SWAP,16)
	s_waitcnt lgkmcnt(0)
	v_add_f32_e32 v98, v98, v102
	v_fmamk_f32 v98, v98, 0x3c000000, v232
	v_rsq_f32_e32 v98, v98
	s_nop 0
	v_mul_f32_e32 v94, v94, v98
	v_mul_f32_e32 v94, v90, v94
	v_cvt_pk_bf16_f32 v94, v94, s0
	ds_write_b16 v193, v94 offset:6528
	v_mul_f32_e32 v94, v97, v98
	v_mul_f32_e32 v94, v89, v94
	v_cvt_pk_bf16_f32 v94, v94, s0
	ds_write_b16 v193, v94 offset:6592
	v_mul_f32_e32 v94, v100, v98
	v_mul_f32_e32 v94, v88, v94
	v_cvt_pk_bf16_f32 v94, v94, s0
	ds_write_b16 v193, v94 offset:6656
	v_mul_f32_e32 v94, v101, v98
	v_mul_f32_e32 v94, v87, v94
	v_cvt_pk_bf16_f32 v94, v94, s0
	ds_write_b16 v193, v94 offset:6720
	v_mul_f32_e32 v94, v63, v69
	v_fma_f32 v86, -v184, v94, v86
	v_mul_f32_e32 v94, v47, v69
	v_fma_f32 v93, -v184, v94, v93
	v_mul_f32_e32 v94, v93, v93
	v_mul_f32_e32 v97, v31, v69
	v_fmac_f32_e32 v94, v86, v86
	v_fma_f32 v96, -v184, v97, v96
	v_mul_f32_e32 v97, v15, v69
	v_fmac_f32_e32 v94, v96, v96
	v_fma_f32 v97, -v184, v97, v99
	v_fmac_f32_e32 v94, v97, v97
	s_nop 1
	v_add_f32_dpp v94, v94, v94 quad_perm:[1,0,3,2] row_mask:0xf bank_mask:0xf bound_ctrl:1
	s_nop 1
	v_add_f32_dpp v94, v94, v94 quad_perm:[2,3,0,1] row_mask:0xf bank_mask:0xf bound_ctrl:1
	s_nop 1
	v_add_f32_dpp v94, v94, v94 row_ror:4 row_mask:0xf bank_mask:0xf bound_ctrl:1
	s_nop 1
	v_add_f32_dpp v94, v94, v94 row_ror:8 row_mask:0xf bank_mask:0xf bound_ctrl:1
	ds_swizzle_b32 v98, v94 offset:swizzle(SWAP,16)
	s_waitcnt lgkmcnt(0)
	v_add_f32_e32 v94, v94, v98
	v_fmamk_f32 v94, v94, 0x3c000000, v232
	v_rsq_f32_e32 v94, v94
	s_nop 0
	v_mul_f32_e32 v86, v86, v94
	v_mul_f32_e32 v86, v90, v86
	v_cvt_pk_bf16_f32 v86, v86, s0
	ds_write_b16 v193, v86 offset:6800
	v_mul_f32_e32 v86, v93, v94
	v_mul_f32_e32 v86, v89, v86
	v_cvt_pk_bf16_f32 v86, v86, s0
	ds_write_b16 v193, v86 offset:6864
	v_mul_f32_e32 v86, v96, v94
	v_mul_f32_e32 v86, v88, v86
	v_cvt_pk_bf16_f32 v86, v86, s0
	ds_write_b16 v193, v86 offset:6928
	v_mul_f32_e32 v86, v97, v94
	v_mul_f32_e32 v86, v87, v86
	v_cvt_pk_bf16_f32 v86, v86, s0
	ds_write_b16 v193, v86 offset:6992
	v_mul_f32_e32 v86, v64, v66
	v_fma_f32 v83, -v184, v86, v83
	v_mul_f32_e32 v86, v48, v66
	v_fma_f32 v85, -v184, v86, v85
	v_mul_f32_e32 v86, v85, v85
	v_mul_f32_e32 v93, v32, v66
	v_fmac_f32_e32 v86, v83, v83
	v_fma_f32 v92, -v184, v93, v92
	v_mul_f32_e32 v93, v16, v66
	v_fmac_f32_e32 v86, v92, v92
	v_fma_f32 v93, -v184, v93, v95
	v_fmac_f32_e32 v86, v93, v93
	s_nop 1
	v_add_f32_dpp v86, v86, v86 quad_perm:[1,0,3,2] row_mask:0xf bank_mask:0xf bound_ctrl:1
	s_nop 1
	v_add_f32_dpp v86, v86, v86 quad_perm:[2,3,0,1] row_mask:0xf bank_mask:0xf bound_ctrl:1
	s_nop 1
	v_add_f32_dpp v86, v86, v86 row_ror:4 row_mask:0xf bank_mask:0xf bound_ctrl:1
	s_nop 1
	v_add_f32_dpp v86, v86, v86 row_ror:8 row_mask:0xf bank_mask:0xf bound_ctrl:1
	ds_swizzle_b32 v94, v86 offset:swizzle(SWAP,16)
	s_waitcnt lgkmcnt(0)
	v_add_f32_e32 v86, v86, v94
	v_fmamk_f32 v86, v86, 0x3c000000, v232
	v_rsq_f32_e32 v86, v86
	s_nop 0
	v_mul_f32_e32 v83, v83, v86
	v_mul_f32_e32 v83, v90, v83
	v_cvt_pk_bf16_f32 v83, v83, s0
	ds_write_b16 v193, v83 offset:7072
	v_mul_f32_e32 v83, v85, v86
	v_mul_f32_e32 v83, v89, v83
	v_cvt_pk_bf16_f32 v83, v83, s0
	ds_write_b16 v193, v83 offset:7136
	v_mul_f32_e32 v83, v92, v86
	v_mul_f32_e32 v83, v88, v83
	v_cvt_pk_bf16_f32 v83, v83, s0
	ds_write_b16 v193, v83 offset:7200
	v_mul_f32_e32 v83, v93, v86
	v_mul_f32_e32 v83, v87, v83
	v_cvt_pk_bf16_f32 v83, v83, s0
	ds_write_b16 v193, v83 offset:7264
	v_mul_f32_e32 v83, v65, v67
	v_fma_f32 v0, -v184, v83, v0
	v_mul_f32_e32 v83, v49, v67
	v_fma_f32 v82, -v184, v83, v82
	v_mul_f32_e32 v83, v82, v82
	v_mul_f32_e32 v85, v33, v67
	v_fmac_f32_e32 v83, v0, v0
	v_fma_f32 v84, -v184, v85, v84
	v_mul_f32_e32 v85, v17, v67
	v_fmac_f32_e32 v83, v84, v84
	v_fma_f32 v85, -v184, v85, v91
	v_fmac_f32_e32 v83, v85, v85
	s_nop 1
	v_add_f32_dpp v83, v83, v83 quad_perm:[1,0,3,2] row_mask:0xf bank_mask:0xf bound_ctrl:1
	s_nop 1
	v_add_f32_dpp v83, v83, v83 quad_perm:[2,3,0,1] row_mask:0xf bank_mask:0xf bound_ctrl:1
	s_nop 1
	v_add_f32_dpp v83, v83, v83 row_ror:4 row_mask:0xf bank_mask:0xf bound_ctrl:1
	s_nop 1
	v_add_f32_dpp v83, v83, v83 row_ror:8 row_mask:0xf bank_mask:0xf bound_ctrl:1
	ds_swizzle_b32 v86, v83 offset:swizzle(SWAP,16)
	s_waitcnt lgkmcnt(0)
	v_add_f32_e32 v83, v83, v86
	v_fmamk_f32 v83, v83, 0x3c000000, v232
	v_rsq_f32_e32 v83, v83
	s_nop 0
	v_mul_f32_e32 v0, v0, v83
	v_mul_f32_e32 v0, v90, v0
	v_cvt_pk_bf16_f32 v0, v0, s0
	ds_write_b16 v193, v0 offset:7344
	v_mul_f32_e32 v0, v82, v83
	v_mul_f32_e32 v0, v89, v0
	v_cvt_pk_bf16_f32 v0, v0, s0
	ds_write_b16 v193, v0 offset:7408
	v_mul_f32_e32 v0, v84, v83
	v_mul_f32_e32 v0, v88, v0
	v_cvt_pk_bf16_f32 v0, v0, s0
	ds_write_b16 v193, v0 offset:7472
	v_mul_f32_e32 v0, v85, v83
	v_mul_f32_e32 v0, v87, v0
	v_cvt_pk_bf16_f32 v0, v0, s0
	ds_write_b16 v193, v0 offset:7536
	v_mov_b64_e32 v[82:83], s[4:5]
	s_waitcnt lgkmcnt(0)
	s_nop 0
	v_lshl_add_u64 v[86:87], v[82:83], 0, v[164:165]
	ds_read_b128 v[82:85], v199
	ds_read_b128 v[212:215], v199 offset:1088
	ds_read_b128 v[216:219], v199 offset:2176
	ds_read_b128 v[228:231], v199 offset:3264
	ds_read_b128 v[244:247], v199 offset:4352
	ds_read_b128 v[248:251], v199 offset:5440
	ds_read_b128 v[106:109], v199 offset:6528
	ds_read_b128 v[110:113], v199 offset:7616
	v_lshl_add_u64 v[88:89], v[86:87], 0, v[166:167]
	s_waitcnt lgkmcnt(7)
	global_store_dwordx4 v[88:89], v[82:85], off
	v_lshl_add_u64 v[88:89], v[86:87], 0, v[168:169]
	s_waitcnt lgkmcnt(6)
	global_store_dwordx4 v[88:89], v[212:215], off
	v_lshl_add_u64 v[88:89], v[86:87], 0, v[170:171]
	s_waitcnt lgkmcnt(5)
	global_store_dwordx4 v[88:89], v[216:219], off
	v_lshl_add_u64 v[88:89], v[86:87], 0, v[172:173]
	s_waitcnt lgkmcnt(4)
	global_store_dwordx4 v[88:89], v[228:231], off
	v_lshl_add_u64 v[88:89], v[86:87], 0, v[174:175]
	s_waitcnt lgkmcnt(3)
	global_store_dwordx4 v[88:89], v[244:247], off
	v_lshl_add_u64 v[88:89], v[86:87], 0, v[176:177]
	s_waitcnt lgkmcnt(2)
	global_store_dwordx4 v[88:89], v[248:251], off
	v_lshl_add_u64 v[88:89], v[86:87], 0, v[178:179]
	v_lshl_add_u64 v[86:87], v[86:87], 0, v[180:181]
	s_waitcnt lgkmcnt(1)
	global_store_dwordx4 v[88:89], v[106:109], off
	s_waitcnt lgkmcnt(0)
	global_store_dwordx4 v[86:87], v[110:113], off
	s_cbranch_execnz .LBB0_1078
	s_branch .LBB0_1127

.LBB0_1612:
	s_add_u32 s36, s34, 0xfffa8080
	s_addc_u32 s37, s35, -1
	s_add_i32 s61, 0, 0x10000
	s_cmp_eq_u32 s60, 18
	s_cselect_b32 s37, s27, s37
	s_cselect_b32 s36, s26, s36
	v_add_u32_e32 v0, s61, v198
	s_cselect_b32 s39, s29, s59
	s_cselect_b32 s38, s28, s31
	s_add_i32 s64, 0, 0x14000
	ds_read_b128 v[130:133], v0
	ds_read_b128 v[134:137], v0 offset:1024
	ds_read_b128 v[138:141], v0 offset:2048
	ds_read_b128 v[142:145], v0 offset:3072
	v_add_u32_e32 v0, s64, v198
	ds_read_b128 v[146:149], v0
	ds_read_b128 v[150:153], v0 offset:1024
	ds_read_b128 v[154:157], v0 offset:2048
	ds_read_b128 v[158:161], v0 offset:3072
	ds_read_b128 v[162:165], v199
	ds_read_b128 v[166:169], v199 offset:1024
	ds_read_b128 v[170:173], v199 offset:2048
	ds_read_b128 v[174:177], v199 offset:3072
	ds_read_b128 v[178:181], v199 offset:4096
	ds_read_b128 v[182:185], v199 offset:5120
	ds_read_b128 v[186:189], v199 offset:6144
	ds_read_b128 v[190:193], v199 offset:7168
	s_add_i32 m0, s85, 0xc000
	s_nop 0
	global_load_lds_dwordx4 v194, s[34:35]
	s_add_i32 m0, s85, 0xe000
	s_nop 0
	global_load_lds_dwordx4 v196, s[34:35]
	s_waitcnt vmcnt(8)
	s_waitcnt lgkmcnt(0)
	s_barrier
	s_setprio 1
	s_waitcnt lgkmcnt(0)
	v_mfma_scale_f32_16x16x128_f8f6f4 v[126:129], v[130:137], v[162:169], v[126:129], v234, v252 op_sel_hi:[0,0,0]
	v_mfma_scale_f32_16x16x128_f8f6f4 v[122:125], v[138:145], v[162:169], v[122:125], v234, v252 op_sel_hi:[0,0,0]
	v_mfma_scale_f32_16x16x128_f8f6f4 v[118:121], v[130:137], v[170:177], v[118:121], v234, v252 op_sel_hi:[0,0,0]
	v_mfma_scale_f32_16x16x128_f8f6f4 v[114:117], v[138:145], v[170:177], v[114:117], v234, v252 op_sel_hi:[0,0,0]
	v_mfma_scale_f32_16x16x128_f8f6f4 v[110:113], v[130:137], v[178:185], v[110:113], v234, v252 op_sel_hi:[0,0,0]
	v_mfma_scale_f32_16x16x128_f8f6f4 v[106:109], v[138:145], v[178:185], v[106:109], v234, v252 op_sel_hi:[0,0,0]
	v_mfma_scale_f32_16x16x128_f8f6f4 v[102:105], v[130:137], v[186:193], v[102:105], v234, v252 op_sel_hi:[0,0,0]
	v_mfma_scale_f32_16x16x128_f8f6f4 v[98:101], v[138:145], v[186:193], v[98:101], v234, v252 op_sel_hi:[0,0,0]
	s_setprio 0
	s_setprio 1
	v_mfma_scale_f32_16x16x128_f8f6f4 v[200:203], v[146:153], v[162:169], v[62:65], v234, v252 op_sel_hi:[0,0,0]
	v_mfma_scale_f32_16x16x128_f8f6f4 v[162:165], v[154:161], v[162:169], v[58:61], v234, v252 op_sel_hi:[0,0,0]
	v_mfma_scale_f32_16x16x128_f8f6f4 v[166:169], v[146:153], v[170:177], v[54:57], v234, v252 op_sel_hi:[0,0,0]
	v_mfma_scale_f32_16x16x128_f8f6f4 v[170:173], v[154:161], v[170:177], v[50:53], v234, v252 op_sel_hi:[0,0,0]
	v_mfma_scale_f32_16x16x128_f8f6f4 v[174:177], v[146:153], v[178:185], v[46:49], v234, v252 op_sel_hi:[0,0,0]
	v_mfma_scale_f32_16x16x128_f8f6f4 v[178:181], v[154:161], v[178:185], v[42:45], v234, v252 op_sel_hi:[0,0,0]
	v_mfma_scale_f32_16x16x128_f8f6f4 v[182:185], v[146:153], v[186:193], v[38:41], v234, v252 op_sel_hi:[0,0,0]
	v_mfma_scale_f32_16x16x128_f8f6f4 v[186:189], v[154:161], v[186:193], v[34:37], v234, v252 op_sel_hi:[0,0,0]
	s_setprio 0
	s_barrier
	s_add_i32 s61, s61, s33
	s_nop 2
	ds_read_b128 v[34:37], v199 offset:16384
	ds_read_b128 v[38:41], v199 offset:17408
	ds_read_b128 v[42:45], v199 offset:18432
	ds_read_b128 v[46:49], v199 offset:19456
	ds_read_b128 v[50:53], v199 offset:20480
	ds_read_b128 v[54:57], v199 offset:21504
	ds_read_b128 v[58:61], v199 offset:22528
	ds_read_b128 v[62:65], v199 offset:23552
	s_mov_b32 m0, s61
	s_nop 0
	global_load_lds_dwordx4 v195, s[38:39]
	s_add_i32 m0, s61, 0x2000
	s_add_u32 s62, s38, 0x58000
	global_load_lds_dwordx4 v197, s[38:39]
	s_addc_u32 s63, s39, 0
	s_add_i32 s61, s64, s33
	s_mov_b32 m0, s61
	s_nop 0
	global_load_lds_dwordx4 v195, s[62:63]
	s_add_i32 m0, s61, 0x2000
	s_nop 0
	global_load_lds_dwordx4 v197, s[62:63]
	s_waitcnt vmcnt(6)
	s_waitcnt lgkmcnt(0)
	s_barrier
	s_setprio 1
	s_waitcnt lgkmcnt(0)
	v_mfma_scale_f32_16x16x128_f8f6f4 v[94:97], v[130:137], v[34:41], v[94:97], v234, v252 op_sel_hi:[0,0,0]
	v_mfma_scale_f32_16x16x128_f8f6f4 v[90:93], v[138:145], v[34:41], v[90:93], v234, v252 op_sel_hi:[0,0,0]
	v_mfma_scale_f32_16x16x128_f8f6f4 v[86:89], v[130:137], v[42:49], v[86:89], v234, v252 op_sel_hi:[0,0,0]
	v_mfma_scale_f32_16x16x128_f8f6f4 v[82:85], v[138:145], v[42:49], v[82:85], v234, v252 op_sel_hi:[0,0,0]
	v_mfma_scale_f32_16x16x128_f8f6f4 v[78:81], v[130:137], v[50:57], v[78:81], v234, v252 op_sel_hi:[0,0,0]
	v_mfma_scale_f32_16x16x128_f8f6f4 v[74:77], v[138:145], v[50:57], v[74:77], v234, v252 op_sel_hi:[0,0,0]
	v_mfma_scale_f32_16x16x128_f8f6f4 v[190:193], v[130:137], v[58:65], v[70:73], v234, v252 op_sel_hi:[0,0,0]
	v_mfma_scale_f32_16x16x128_f8f6f4 v[204:207], v[138:145], v[58:65], v[66:69], v234, v252 op_sel_hi:[0,0,0]
	s_setprio 0
	s_setprio 1
	v_mfma_scale_f32_16x16x128_f8f6f4 v[208:211], v[146:153], v[34:41], v[30:33], v234, v252 op_sel_hi:[0,0,0]
	v_mfma_scale_f32_16x16x128_f8f6f4 v[212:215], v[154:161], v[34:41], v[26:29], v234, v252 op_sel_hi:[0,0,0]
	v_mfma_scale_f32_16x16x128_f8f6f4 v[216:219], v[146:153], v[42:49], v[22:25], v234, v252 op_sel_hi:[0,0,0]
	v_mfma_scale_f32_16x16x128_f8f6f4 v[228:231], v[154:161], v[42:49], v[18:21], v234, v252 op_sel_hi:[0,0,0]
	v_mfma_scale_f32_16x16x128_f8f6f4 v[244:247], v[146:153], v[50:57], v[14:17], v234, v252 op_sel_hi:[0,0,0]
	v_mfma_scale_f32_16x16x128_f8f6f4 v[248:251], v[154:161], v[50:57], v[10:13], v234, v252 op_sel_hi:[0,0,0]
	v_mfma_scale_f32_16x16x128_f8f6f4 v[224:227], v[146:153], v[58:65], v[6:9], v234, v252 op_sel_hi:[0,0,0]
	v_mfma_scale_f32_16x16x128_f8f6f4 v[220:223], v[154:161], v[58:65], v[2:5], v234, v252 op_sel_hi:[0,0,0]
	s_setprio 0
	s_barrier
	s_add_i32 s61, 0, 0x18000
	v_add_u32_e32 v0, s61, v198
	s_add_i32 s64, 0, 0x1c000
	s_nop 1
	ds_read_b128 v[2:5], v0
	ds_read_b128 v[6:9], v0 offset:1024
	ds_read_b128 v[10:13], v0 offset:2048
	ds_read_b128 v[14:17], v0 offset:3072
	v_add_u32_e32 v0, s64, v198
	ds_read_b128 v[130:133], v0
	ds_read_b128 v[134:137], v0 offset:1024
	ds_read_b128 v[138:141], v0 offset:2048
	ds_read_b128 v[142:145], v0 offset:3072
	s_add_u32 s62, s36, 0x58000
	ds_read_b128 v[18:21], v199 offset:32768
	ds_read_b128 v[22:25], v199 offset:33792
	ds_read_b128 v[26:29], v199 offset:34816
	ds_read_b128 v[30:33], v199 offset:35840
	ds_read_b128 v[34:37], v199 offset:36864
	ds_read_b128 v[38:41], v199 offset:37888
	ds_read_b128 v[66:69], v199 offset:38912
	ds_read_b128 v[70:73], v199 offset:39936
	s_addc_u32 s63, s37, 0
	s_mov_b32 m0, s85
	s_nop 0
	global_load_lds_dwordx4 v194, s[36:37]
	s_mov_b32 m0, s3
	s_nop 0
	global_load_lds_dwordx4 v196, s[36:37]
	s_mov_b32 m0, s45
	s_nop 0
	global_load_lds_dwordx4 v194, s[62:63]
	s_mov_b32 m0, s47
	s_nop 0
	global_load_lds_dwordx4 v196, s[62:63]
	s_waitcnt vmcnt(8)
	s_waitcnt lgkmcnt(0)
	s_barrier
	s_setprio 1
	s_waitcnt lgkmcnt(0)
	v_mfma_scale_f32_16x16x128_f8f6f4 v[126:129], v[2:9], v[18:25], v[126:129], v234, v252 op_sel_hi:[0,0,0]
	v_mfma_scale_f32_16x16x128_f8f6f4 v[122:125], v[10:17], v[18:25], v[122:125], v234, v252 op_sel_hi:[0,0,0]
	v_mfma_scale_f32_16x16x128_f8f6f4 v[118:121], v[2:9], v[26:33], v[118:121], v234, v252 op_sel_hi:[0,0,0]
	v_mfma_scale_f32_16x16x128_f8f6f4 v[114:117], v[10:17], v[26:33], v[114:117], v234, v252 op_sel_hi:[0,0,0]
	v_mfma_scale_f32_16x16x128_f8f6f4 v[110:113], v[2:9], v[34:41], v[110:113], v234, v252 op_sel_hi:[0,0,0]
	v_mfma_scale_f32_16x16x128_f8f6f4 v[106:109], v[10:17], v[34:41], v[106:109], v234, v252 op_sel_hi:[0,0,0]
	v_mfma_scale_f32_16x16x128_f8f6f4 v[102:105], v[2:9], v[66:73], v[102:105], v234, v252 op_sel_hi:[0,0,0]
	v_mfma_scale_f32_16x16x128_f8f6f4 v[98:101], v[10:17], v[66:73], v[98:101], v234, v252 op_sel_hi:[0,0,0]
	s_setprio 0
	s_setprio 1
	v_mfma_scale_f32_16x16x128_f8f6f4 v[62:65], v[130:137], v[18:25], v[200:203], v234, v252 op_sel_hi:[0,0,0]
	v_mfma_scale_f32_16x16x128_f8f6f4 v[58:61], v[138:145], v[18:25], v[162:165], v234, v252 op_sel_hi:[0,0,0]
	v_mfma_scale_f32_16x16x128_f8f6f4 v[54:57], v[130:137], v[26:33], v[166:169], v234, v252 op_sel_hi:[0,0,0]
	v_mfma_scale_f32_16x16x128_f8f6f4 v[50:53], v[138:145], v[26:33], v[170:173], v234, v252 op_sel_hi:[0,0,0]
	v_mfma_scale_f32_16x16x128_f8f6f4 v[46:49], v[130:137], v[34:41], v[174:177], v234, v252 op_sel_hi:[0,0,0]
	v_mfma_scale_f32_16x16x128_f8f6f4 v[42:45], v[138:145], v[34:41], v[178:181], v234, v252 op_sel_hi:[0,0,0]
	v_mfma_scale_f32_16x16x128_f8f6f4 v[38:41], v[130:137], v[66:73], v[182:185], v234, v252 op_sel_hi:[0,0,0]
	v_mfma_scale_f32_16x16x128_f8f6f4 v[34:37], v[138:145], v[66:73], v[186:189], v234, v252 op_sel_hi:[0,0,0]
	s_setprio 0
	s_barrier
	v_mov_b32_e32 v0, v195
	ds_read_b128 v[18:21], v199 offset:49152
	ds_read_b128 v[22:25], v199 offset:50176
	ds_read_b128 v[146:149], v199 offset:51200
	ds_read_b128 v[150:153], v199 offset:52224
	ds_read_b128 v[154:157], v199 offset:53248
	ds_read_b128 v[158:161], v199 offset:54272
	ds_read_b128 v[162:165], v199 offset:55296
	ds_read_b128 v[166:169], v199 offset:56320
	s_add_i32 s61, s61, s33
	v_lshl_add_u64 v[26:27], s[38:39], 0, v[0:1]
	v_lshl_add_u64 v[26:27], v[26:27], 0, s[90:91]
	s_mov_b32 m0, s61
	v_mov_b32_e32 v0, v197
	global_load_lds_dwordx4 v[26:27], off
	s_add_i32 m0, s61, 0x2000
	s_nop 0
	v_lshl_add_u64 v[26:27], s[38:39], 0, v[0:1]
	s_add_u32 s38, s38, 0x58080
	v_lshl_add_u64 v[26:27], v[26:27], 0, s[90:91]
	s_addc_u32 s39, s39, 0
	s_add_i32 s61, s64, s33
	global_load_lds_dwordx4 v[26:27], off
	s_mov_b32 m0, s61
	s_nop 0
	global_load_lds_dwordx4 v195, s[38:39]
	s_add_i32 m0, s61, 0x2000
	s_nop 0
	global_load_lds_dwordx4 v197, s[38:39]
	s_waitcnt vmcnt(6)
	s_waitcnt lgkmcnt(0)
	s_barrier
	s_setprio 1
	s_waitcnt lgkmcnt(0)
	v_mfma_scale_f32_16x16x128_f8f6f4 v[94:97], v[2:9], v[18:25], v[94:97], v234, v252 op_sel_hi:[0,0,0]
	v_mfma_scale_f32_16x16x128_f8f6f4 v[90:93], v[10:17], v[18:25], v[90:93], v234, v252 op_sel_hi:[0,0,0]
	v_mfma_scale_f32_16x16x128_f8f6f4 v[86:89], v[2:9], v[146:153], v[86:89], v234, v252 op_sel_hi:[0,0,0]
	v_mfma_scale_f32_16x16x128_f8f6f4 v[82:85], v[10:17], v[146:153], v[82:85], v234, v252 op_sel_hi:[0,0,0]
	v_mfma_scale_f32_16x16x128_f8f6f4 v[78:81], v[2:9], v[154:161], v[78:81], v234, v252 op_sel_hi:[0,0,0]
	v_mfma_scale_f32_16x16x128_f8f6f4 v[74:77], v[10:17], v[154:161], v[74:77], v234, v252 op_sel_hi:[0,0,0]
	v_mfma_scale_f32_16x16x128_f8f6f4 v[70:73], v[2:9], v[162:169], v[190:193], v234, v252 op_sel_hi:[0,0,0]
	v_mfma_scale_f32_16x16x128_f8f6f4 v[66:69], v[10:17], v[162:169], v[204:207], v234, v252 op_sel_hi:[0,0,0]
	s_setprio 0
	s_setprio 1
	v_mfma_scale_f32_16x16x128_f8f6f4 v[30:33], v[130:137], v[18:25], v[208:211], v234, v252 op_sel_hi:[0,0,0]
	v_mfma_scale_f32_16x16x128_f8f6f4 v[26:29], v[138:145], v[18:25], v[212:215], v234, v252 op_sel_hi:[0,0,0]
	v_mfma_scale_f32_16x16x128_f8f6f4 v[22:25], v[130:137], v[146:153], v[216:219], v234, v252 op_sel_hi:[0,0,0]
	v_mfma_scale_f32_16x16x128_f8f6f4 v[18:21], v[138:145], v[146:153], v[228:231], v234, v252 op_sel_hi:[0,0,0]
	v_mfma_scale_f32_16x16x128_f8f6f4 v[14:17], v[130:137], v[154:161], v[244:247], v234, v252 op_sel_hi:[0,0,0]
	v_mfma_scale_f32_16x16x128_f8f6f4 v[10:13], v[138:145], v[154:161], v[248:251], v234, v252 op_sel_hi:[0,0,0]
	v_mfma_scale_f32_16x16x128_f8f6f4 v[6:9], v[130:137], v[162:169], v[224:227], v234, v252 op_sel_hi:[0,0,0]
	v_mfma_scale_f32_16x16x128_f8f6f4 v[2:5], v[138:145], v[162:169], v[220:223], v234, v252 op_sel_hi:[0,0,0]
	s_setprio 0
	s_barrier
	v_mov_b32_e32 v0, v194
	s_mov_b32 m0, s50
	v_lshl_add_u64 v[190:191], s[36:37], 0, v[0:1]
	v_lshl_add_u64 v[190:191], v[190:191], 0, s[90:91]
	v_mov_b32_e32 v0, v196
	global_load_lds_dwordx4 v[190:191], off
	s_mov_b32 m0, s51
	v_lshl_add_u64 v[190:191], s[36:37], 0, v[0:1]
	v_lshl_add_u64 v[190:191], v[190:191], 0, s[90:91]
	global_load_lds_dwordx4 v[190:191], off
	s_add_i32 s60, s60, 2
	s_add_u32 s34, s34, 0x100
	s_addc_u32 s35, s35, 0
	s_add_u32 s31, s31, 0x100
	s_addc_u32 s59, s59, 0
	s_cmp_gt_u32 s60, 19
	s_cbranch_scc0 .LBB0_1612
	v_readlane_b32 s34, v254, 19
	v_readlane_b32 s35, v254, 20
	s_and_b64 vcc, exec, s[34:35]
	s_lshl_b32 s31, s30, 8
	s_ashr_i32 s30, s30, 3
	s_add_i32 s34, s31, s87
	s_mul_hi_i32 s31, s30, 0x6000
	s_mulk_i32 s30, 0x6000
	s_add_u32 s30, s48, s30
	v_mbcnt_lo_u32_b32 v0, -1, 0
	v_mbcnt_hi_u32_b32 v0, -1, v0
	s_addc_u32 s31, s49, s31
	s_lshl_b32 s35, s58, 8
	v_lshrrev_b32_e32 v130, 1, v0
	v_and_or_b32 v130, v130, 24, s35
	v_or_b32_e32 v138, s72, v130
	v_ashrrev_i32_e32 v139, 31, v138
	v_lshl_add_u64 v[140:141], v[138:139], 2, s[30:31]
	global_load_dwordx4 v[130:133], v[140:141], off offset:16
	global_load_dwordx4 v[134:137], v[140:141], off
	s_cbranch_vccz .LBB0_1615
	s_barrier
.LBB0_1615:
	v_lshlrev_b64 v[180:181], 1, v[138:139]
	s_mov_b64 s[30:31], 0x40000
	v_or_b32_e32 v168, 0x80, v138
	v_ashrrev_i32_e32 v169, 31, v168
	s_and_b64 vcc, exec, s[8:9]
	s_mov_b64 s[64:65], 0x15020080
	s_waitcnt vmcnt(0)
	v_pk_add_f32 v[172:173], v[132:133], 1.0 op_sel_hi:[1,0]
	v_pk_add_f32 v[176:177], v[136:137], 1.0 op_sel_hi:[1,0]
	v_pk_add_f32 v[178:179], v[134:135], 1.0 op_sel_hi:[1,0]
	v_pk_add_f32 v[174:175], v[130:131], 1.0 op_sel_hi:[1,0]
	global_load_dwordx4 v[130:133], v[140:141], off offset:528
	global_load_dwordx4 v[134:137], v[140:141], off offset:512
	s_waitcnt vmcnt(1)
	v_pk_add_f32 v[158:159], v[130:131], 1.0 op_sel_hi:[1,0]
	v_and_or_b32 v130, v0, 15, s34
	v_ashrrev_i32_e32 v131, 31, v130
	v_pk_add_f32 v[160:161], v[132:133], 1.0 op_sel_hi:[1,0]
	v_lshl_add_u64 v[132:133], s[18:19], 0, v[180:181]
	v_lshlrev_b64 v[166:167], 11, v[130:131]
	s_waitcnt vmcnt(0)
	v_pk_add_f32 v[162:163], v[134:135], 1.0 op_sel_hi:[1,0]
	v_lshl_add_u64 v[134:135], v[132:133], 0, v[166:167]
	global_load_dwordx4 v[200:203], v[134:135], off
	v_or_b32_e32 v134, 16, v130
	v_ashrrev_i32_e32 v135, 31, v134
	v_lshlrev_b64 v[204:205], 11, v[134:135]
	v_lshl_add_u64 v[134:135], v[132:133], 0, v[204:205]
	global_load_dwordx4 v[154:157], v[134:135], off
	v_or_b32_e32 v134, 32, v130
	v_ashrrev_i32_e32 v135, 31, v134
	v_lshlrev_b64 v[192:193], 11, v[134:135]
	v_or_b32_e32 v130, 48, v130
	v_lshl_add_u64 v[134:135], v[132:133], 0, v[192:193]
	v_ashrrev_i32_e32 v131, 31, v130
	global_load_dwordx4 v[150:153], v[134:135], off
	v_lshlrev_b64 v[190:191], 11, v[130:131]
	v_lshl_add_u64 v[130:131], v[132:133], 0, v[190:191]
	global_load_dwordx4 v[146:149], v[130:131], off
	v_lshl_add_u64 v[188:189], v[166:167], 0, s[30:31]
	v_lshl_add_u64 v[130:131], v[132:133], 0, v[188:189]
	s_mov_b64 s[30:31], 0x48000
	global_load_dwordx4 v[142:145], v[130:131], off
	v_lshl_add_u64 v[184:185], v[166:167], 0, s[30:31]
	v_lshl_add_u64 v[130:131], v[132:133], 0, v[184:185]
	s_mov_b64 s[30:31], 0x50000
	v_pk_add_f32 v[164:165], v[136:137], 1.0 op_sel_hi:[1,0]
	global_load_dwordx4 v[134:137], v[130:131], off
	v_lshl_add_u64 v[186:187], v[166:167], 0, s[30:31]
	v_lshl_add_u64 v[130:131], v[132:133], 0, v[186:187]
	s_mov_b64 s[30:31], 0x58000
	global_load_dwordx4 v[138:141], v[130:131], off
	v_lshl_add_u64 v[182:183], v[166:167], 0, s[30:31]
	v_lshl_add_u64 v[130:131], v[132:133], 0, v[182:183]
	global_load_dwordx4 v[130:133], v[130:131], off
	v_lshl_add_u64 v[170:171], s[18:19], 0, v[166:167]
	v_lshl_add_u64 v[166:167], v[170:171], 0, v[180:181]
	s_mov_b64 s[30:31], -1
	s_waitcnt vmcnt(7)
	v_lshlrev_b32_e32 v206, 16, v200
	v_and_b32_e32 v207, 0xffff0000, v200
	v_lshlrev_b32_e32 v200, 16, v201
	v_and_b32_e32 v201, 0xffff0000, v201
	v_pk_fma_f32 v[128:129], v[128:129], v[176:177], v[200:201]
	v_pk_fma_f32 v[126:127], v[126:127], v[178:179], v[206:207]
	v_lshlrev_b32_e32 v200, 16, v202
	v_and_b32_e32 v201, 0xffff0000, v202
	v_lshlrev_b32_e32 v202, 16, v203
	v_and_b32_e32 v203, 0xffff0000, v203
	v_pk_fma_f32 v[202:203], v[124:125], v[172:173], v[202:203]
	v_pk_fma_f32 v[124:125], v[122:123], v[174:175], v[200:201]
	v_cvt_pk_bf16_f32 v122, v126, v127
	v_cvt_pk_bf16_f32 v123, v128, v129
	s_waitcnt vmcnt(6)
	v_lshlrev_b32_e32 v126, 16, v154
	v_and_b32_e32 v127, 0xffff0000, v154
	v_lshlrev_b32_e32 v128, 16, v155
	v_and_b32_e32 v129, 0xffff0000, v155
	v_cvt_pk_bf16_f32 v124, v124, v125
	v_cvt_pk_bf16_f32 v125, v202, v203
	v_pk_fma_f32 v[120:121], v[120:121], v[176:177], v[128:129]
	v_pk_fma_f32 v[118:119], v[118:119], v[178:179], v[126:127]
	v_lshlrev_b32_e32 v126, 16, v156
	v_and_b32_e32 v127, 0xffff0000, v156
	v_lshlrev_b32_e32 v128, 16, v157
	v_and_b32_e32 v129, 0xffff0000, v157
	global_store_dwordx4 v[166:167], v[122:125], off
	v_pk_fma_f32 v[128:129], v[116:117], v[172:173], v[128:129]
	v_pk_fma_f32 v[116:117], v[114:115], v[174:175], v[126:127]
	v_lshl_add_u64 v[124:125], s[18:19], 0, v[204:205]
	v_cvt_pk_bf16_f32 v114, v118, v119
	v_cvt_pk_bf16_f32 v115, v120, v121
	s_waitcnt vmcnt(6)
	v_lshlrev_b32_e32 v118, 16, v150
	v_and_b32_e32 v119, 0xffff0000, v150
	v_lshlrev_b32_e32 v120, 16, v151
	v_and_b32_e32 v121, 0xffff0000, v151
	v_lshl_add_u64 v[122:123], v[124:125], 0, v[180:181]
	v_cvt_pk_bf16_f32 v116, v116, v117
	v_cvt_pk_bf16_f32 v117, v128, v129
	v_pk_fma_f32 v[112:113], v[112:113], v[176:177], v[120:121]
	v_pk_fma_f32 v[110:111], v[110:111], v[178:179], v[118:119]
	v_lshlrev_b32_e32 v118, 16, v152
	v_and_b32_e32 v119, 0xffff0000, v152
	v_lshlrev_b32_e32 v120, 16, v153
	v_and_b32_e32 v121, 0xffff0000, v153
	global_store_dwordx4 v[122:123], v[114:117], off
	v_pk_fma_f32 v[120:121], v[108:109], v[172:173], v[120:121]
	v_pk_fma_f32 v[108:109], v[106:107], v[174:175], v[118:119]
	v_lshl_add_u64 v[116:117], s[18:19], 0, v[192:193]
	v_cvt_pk_bf16_f32 v106, v110, v111
	v_cvt_pk_bf16_f32 v107, v112, v113
	s_waitcnt vmcnt(6)
	v_lshlrev_b32_e32 v110, 16, v146
	v_and_b32_e32 v111, 0xffff0000, v146
	v_lshlrev_b32_e32 v112, 16, v147
	v_and_b32_e32 v113, 0xffff0000, v147
	v_lshl_add_u64 v[114:115], v[116:117], 0, v[180:181]
	v_cvt_pk_bf16_f32 v108, v108, v109
	v_cvt_pk_bf16_f32 v109, v120, v121
	v_pk_fma_f32 v[104:105], v[104:105], v[176:177], v[112:113]
	v_pk_fma_f32 v[102:103], v[102:103], v[178:179], v[110:111]
	v_lshlrev_b32_e32 v110, 16, v148
	v_and_b32_e32 v111, 0xffff0000, v148
	v_lshlrev_b32_e32 v112, 16, v149
	v_and_b32_e32 v113, 0xffff0000, v149
	global_store_dwordx4 v[114:115], v[106:109], off
	v_pk_fma_f32 v[112:113], v[100:101], v[172:173], v[112:113]
	v_pk_fma_f32 v[100:101], v[98:99], v[174:175], v[110:111]
	v_lshl_add_u64 v[108:109], s[18:19], 0, v[190:191]
	v_cvt_pk_bf16_f32 v98, v102, v103
	v_cvt_pk_bf16_f32 v99, v104, v105
	s_waitcnt vmcnt(6)
	v_lshlrev_b32_e32 v102, 16, v142
	v_and_b32_e32 v103, 0xffff0000, v142
	v_lshlrev_b32_e32 v104, 16, v143
	v_and_b32_e32 v105, 0xffff0000, v143
	v_lshl_add_u64 v[106:107], v[108:109], 0, v[180:181]
	v_cvt_pk_bf16_f32 v100, v100, v101
	v_cvt_pk_bf16_f32 v101, v112, v113
	v_pk_fma_f32 v[96:97], v[96:97], v[176:177], v[104:105]
	v_pk_fma_f32 v[94:95], v[94:95], v[178:179], v[102:103]
	v_lshlrev_b32_e32 v102, 16, v144
	v_and_b32_e32 v103, 0xffff0000, v144
	v_lshlrev_b32_e32 v104, 16, v145
	v_and_b32_e32 v105, 0xffff0000, v145
	global_store_dwordx4 v[106:107], v[98:101], off
	v_pk_fma_f32 v[104:105], v[92:93], v[172:173], v[104:105]
	v_pk_fma_f32 v[92:93], v[90:91], v[174:175], v[102:103]
	v_lshl_add_u64 v[100:101], s[18:19], 0, v[188:189]
	v_cvt_pk_bf16_f32 v90, v94, v95
	v_cvt_pk_bf16_f32 v91, v96, v97
	s_waitcnt vmcnt(6)
	v_lshlrev_b32_e32 v94, 16, v134
	v_and_b32_e32 v95, 0xffff0000, v134
	v_lshlrev_b32_e32 v96, 16, v135
	v_and_b32_e32 v97, 0xffff0000, v135
	v_lshl_add_u64 v[98:99], v[100:101], 0, v[180:181]
	v_cvt_pk_bf16_f32 v92, v92, v93
	v_cvt_pk_bf16_f32 v93, v104, v105
	v_pk_fma_f32 v[88:89], v[88:89], v[176:177], v[96:97]
	v_pk_fma_f32 v[86:87], v[86:87], v[178:179], v[94:95]
	v_lshlrev_b32_e32 v94, 16, v136
	v_and_b32_e32 v95, 0xffff0000, v136
	v_lshlrev_b32_e32 v96, 16, v137
	v_and_b32_e32 v97, 0xffff0000, v137
	global_store_dwordx4 v[98:99], v[90:93], off
	v_pk_fma_f32 v[96:97], v[84:85], v[172:173], v[96:97]
	v_pk_fma_f32 v[84:85], v[82:83], v[174:175], v[94:95]
	v_lshl_add_u64 v[92:93], s[18:19], 0, v[184:185]
	v_cvt_pk_bf16_f32 v82, v86, v87
	v_cvt_pk_bf16_f32 v83, v88, v89
	s_waitcnt vmcnt(6)
	v_lshlrev_b32_e32 v86, 16, v138
	v_and_b32_e32 v87, 0xffff0000, v138
	v_lshlrev_b32_e32 v88, 16, v139
	v_and_b32_e32 v89, 0xffff0000, v139
	v_lshl_add_u64 v[90:91], v[92:93], 0, v[180:181]
	v_cvt_pk_bf16_f32 v84, v84, v85
	v_cvt_pk_bf16_f32 v85, v96, v97
	v_pk_fma_f32 v[80:81], v[80:81], v[176:177], v[88:89]
	v_pk_fma_f32 v[78:79], v[78:79], v[178:179], v[86:87]
	v_lshlrev_b32_e32 v86, 16, v140
	v_and_b32_e32 v87, 0xffff0000, v140
	v_lshlrev_b32_e32 v88, 16, v141
	v_and_b32_e32 v89, 0xffff0000, v141
	global_store_dwordx4 v[90:91], v[82:85], off
	v_pk_fma_f32 v[88:89], v[76:77], v[172:173], v[88:89]
	v_pk_fma_f32 v[76:77], v[74:75], v[174:175], v[86:87]
	v_lshl_add_u64 v[84:85], s[18:19], 0, v[186:187]
	v_cvt_pk_bf16_f32 v74, v78, v79
	v_cvt_pk_bf16_f32 v75, v80, v81
	s_waitcnt vmcnt(6)
	v_lshlrev_b32_e32 v78, 16, v130
	v_and_b32_e32 v79, 0xffff0000, v130
	v_lshlrev_b32_e32 v80, 16, v131
	v_and_b32_e32 v81, 0xffff0000, v131
	v_lshl_add_u64 v[82:83], v[84:85], 0, v[180:181]
	v_cvt_pk_bf16_f32 v76, v76, v77
	v_cvt_pk_bf16_f32 v77, v88, v89
	v_pk_fma_f32 v[72:73], v[72:73], v[176:177], v[80:81]
	v_pk_fma_f32 v[70:71], v[70:71], v[178:179], v[78:79]
	v_lshlrev_b32_e32 v78, 16, v132
	v_and_b32_e32 v79, 0xffff0000, v132
	v_lshlrev_b32_e32 v80, 16, v133
	v_and_b32_e32 v81, 0xffff0000, v133
	global_store_dwordx4 v[82:83], v[74:77], off
	v_pk_fma_f32 v[80:81], v[68:69], v[172:173], v[80:81]
	v_pk_fma_f32 v[68:69], v[66:67], v[174:175], v[78:79]
	v_lshl_add_u64 v[76:77], s[18:19], 0, v[182:183]
	v_lshl_add_u64 v[74:75], v[76:77], 0, v[180:181]
	v_cvt_pk_bf16_f32 v66, v70, v71
	v_cvt_pk_bf16_f32 v67, v72, v73
	v_cvt_pk_bf16_f32 v68, v68, v69
	v_cvt_pk_bf16_f32 v69, v80, v81
	v_lshlrev_b64 v[78:79], 1, v[168:169]
	global_store_dwordx4 v[74:75], v[66:69], off
	v_lshl_add_u64 v[70:71], v[124:125], 0, v[78:79]
	global_load_dwordx4 v[70:73], v[70:71], off
	v_lshl_add_u64 v[66:67], v[170:171], 0, v[78:79]
	global_load_dwordx4 v[66:69], v[66:67], off
	v_lshl_add_u64 v[80:81], v[116:117], 0, v[78:79]
	global_load_dwordx4 v[86:89], v[80:81], off
	v_lshl_add_u64 v[80:81], v[108:109], 0, v[78:79]
	global_load_dwordx4 v[94:97], v[80:81], off
	v_lshl_add_u64 v[80:81], v[100:101], 0, v[78:79]
	global_load_dwordx4 v[100:103], v[80:81], off
	v_lshl_add_u64 v[80:81], v[92:93], 0, v[78:79]
	global_load_dwordx4 v[108:111], v[80:81], off
	v_lshl_add_u64 v[80:81], v[84:85], 0, v[78:79]
	global_load_dwordx4 v[116:119], v[80:81], off
	v_lshl_add_u64 v[76:77], v[76:77], 0, v[78:79]
	global_load_dwordx4 v[76:79], v[76:77], off
	s_waitcnt vmcnt(6)
	v_lshlrev_b32_e32 v80, 16, v66
	v_and_b32_e32 v81, 0xffff0000, v66
	v_lshlrev_b32_e32 v66, 16, v67
	v_and_b32_e32 v67, 0xffff0000, v67
	v_pk_fma_f32 v[64:65], v[64:65], v[164:165], v[66:67]
	v_lshlrev_b32_e32 v66, 16, v68
	v_and_b32_e32 v67, 0xffff0000, v68
	v_lshlrev_b32_e32 v68, 16, v69
	v_and_b32_e32 v69, 0xffff0000, v69
	v_pk_fma_f32 v[62:63], v[62:63], v[162:163], v[80:81]
	v_pk_fma_f32 v[68:69], v[60:61], v[160:161], v[68:69]
	v_pk_fma_f32 v[60:61], v[58:59], v[158:159], v[66:67]
	v_cvt_pk_bf16_f32 v58, v62, v63
	v_cvt_pk_bf16_f32 v59, v64, v65
	v_cvt_pk_bf16_f32 v60, v60, v61
	v_cvt_pk_bf16_f32 v61, v68, v69
	global_store_dwordx4 v[166:167], v[58:61], off offset:256
	s_nop 1
	v_lshlrev_b32_e32 v58, 16, v70
	v_and_b32_e32 v59, 0xffff0000, v70
	v_lshlrev_b32_e32 v60, 16, v71
	v_and_b32_e32 v61, 0xffff0000, v71
	v_pk_fma_f32 v[56:57], v[56:57], v[164:165], v[60:61]
	v_pk_fma_f32 v[54:55], v[54:55], v[162:163], v[58:59]
	v_lshlrev_b32_e32 v58, 16, v72
	v_and_b32_e32 v59, 0xffff0000, v72
	v_lshlrev_b32_e32 v60, 16, v73
	v_and_b32_e32 v61, 0xffff0000, v73
	v_pk_fma_f32 v[60:61], v[52:53], v[160:161], v[60:61]
	v_pk_fma_f32 v[52:53], v[50:51], v[158:159], v[58:59]
	v_cvt_pk_bf16_f32 v50, v54, v55
	v_cvt_pk_bf16_f32 v51, v56, v57
	v_cvt_pk_bf16_f32 v52, v52, v53
	v_cvt_pk_bf16_f32 v53, v60, v61
	global_store_dwordx4 v[122:123], v[50:53], off offset:256
	s_waitcnt vmcnt(7)
	s_nop 0
	v_lshlrev_b32_e32 v50, 16, v86
	v_and_b32_e32 v51, 0xffff0000, v86
	v_lshlrev_b32_e32 v52, 16, v87
	v_and_b32_e32 v53, 0xffff0000, v87
	v_pk_fma_f32 v[48:49], v[48:49], v[164:165], v[52:53]
	v_pk_fma_f32 v[46:47], v[46:47], v[162:163], v[50:51]
	v_lshlrev_b32_e32 v50, 16, v88
	v_and_b32_e32 v51, 0xffff0000, v88
	v_lshlrev_b32_e32 v52, 16, v89
	v_and_b32_e32 v53, 0xffff0000, v89
	v_pk_fma_f32 v[52:53], v[44:45], v[160:161], v[52:53]
	v_pk_fma_f32 v[44:45], v[42:43], v[158:159], v[50:51]
	v_cvt_pk_bf16_f32 v42, v46, v47
	v_cvt_pk_bf16_f32 v43, v48, v49
	v_cvt_pk_bf16_f32 v44, v44, v45
	v_cvt_pk_bf16_f32 v45, v52, v53
	global_store_dwordx4 v[114:115], v[42:45], off offset:256
	s_waitcnt vmcnt(7)
	s_nop 0
	v_lshlrev_b32_e32 v42, 16, v94
	v_and_b32_e32 v43, 0xffff0000, v94
	v_lshlrev_b32_e32 v44, 16, v95
	v_and_b32_e32 v45, 0xffff0000, v95
	v_pk_fma_f32 v[40:41], v[40:41], v[164:165], v[44:45]
	v_pk_fma_f32 v[38:39], v[38:39], v[162:163], v[42:43]
	v_lshlrev_b32_e32 v42, 16, v96
	v_and_b32_e32 v43, 0xffff0000, v96
	v_lshlrev_b32_e32 v44, 16, v97
	v_and_b32_e32 v45, 0xffff0000, v97
	v_pk_fma_f32 v[44:45], v[36:37], v[160:161], v[44:45]
	v_pk_fma_f32 v[36:37], v[34:35], v[158:159], v[42:43]
	v_cvt_pk_bf16_f32 v34, v38, v39
	v_cvt_pk_bf16_f32 v35, v40, v41
	v_cvt_pk_bf16_f32 v36, v36, v37
	v_cvt_pk_bf16_f32 v37, v44, v45
	global_store_dwordx4 v[106:107], v[34:37], off offset:256
	s_waitcnt vmcnt(7)
	s_nop 0
	v_lshlrev_b32_e32 v34, 16, v100
	v_and_b32_e32 v35, 0xffff0000, v100
	v_lshlrev_b32_e32 v36, 16, v101
	v_and_b32_e32 v37, 0xffff0000, v101
	v_pk_fma_f32 v[32:33], v[32:33], v[164:165], v[36:37]
	v_pk_fma_f32 v[30:31], v[30:31], v[162:163], v[34:35]
	v_lshlrev_b32_e32 v34, 16, v102
	v_and_b32_e32 v35, 0xffff0000, v102
	v_lshlrev_b32_e32 v36, 16, v103
	v_and_b32_e32 v37, 0xffff0000, v103
	v_pk_fma_f32 v[36:37], v[28:29], v[160:161], v[36:37]
	v_pk_fma_f32 v[28:29], v[26:27], v[158:159], v[34:35]
	v_cvt_pk_bf16_f32 v26, v30, v31
	v_cvt_pk_bf16_f32 v27, v32, v33
	v_cvt_pk_bf16_f32 v28, v28, v29
	v_cvt_pk_bf16_f32 v29, v36, v37
	global_store_dwordx4 v[98:99], v[26:29], off offset:256
	s_waitcnt vmcnt(7)
	s_nop 0
	v_lshlrev_b32_e32 v26, 16, v108
	v_and_b32_e32 v27, 0xffff0000, v108
	v_lshlrev_b32_e32 v28, 16, v109
	v_and_b32_e32 v29, 0xffff0000, v109
	v_pk_fma_f32 v[24:25], v[24:25], v[164:165], v[28:29]
	v_pk_fma_f32 v[22:23], v[22:23], v[162:163], v[26:27]
	v_lshlrev_b32_e32 v26, 16, v110
	v_and_b32_e32 v27, 0xffff0000, v110
	v_lshlrev_b32_e32 v28, 16, v111
	v_and_b32_e32 v29, 0xffff0000, v111
	v_pk_fma_f32 v[28:29], v[20:21], v[160:161], v[28:29]
	v_pk_fma_f32 v[20:21], v[18:19], v[158:159], v[26:27]
	v_cvt_pk_bf16_f32 v18, v22, v23
	v_cvt_pk_bf16_f32 v19, v24, v25
	v_cvt_pk_bf16_f32 v20, v20, v21
	v_cvt_pk_bf16_f32 v21, v28, v29
	global_store_dwordx4 v[90:91], v[18:21], off offset:256
	s_waitcnt vmcnt(7)
	s_nop 0
	v_lshlrev_b32_e32 v18, 16, v116
	v_and_b32_e32 v19, 0xffff0000, v116
	v_lshlrev_b32_e32 v20, 16, v117
	v_and_b32_e32 v21, 0xffff0000, v117
	v_pk_fma_f32 v[16:17], v[16:17], v[164:165], v[20:21]
	v_pk_fma_f32 v[14:15], v[14:15], v[162:163], v[18:19]
	v_lshlrev_b32_e32 v18, 16, v118
	v_and_b32_e32 v19, 0xffff0000, v118
	v_lshlrev_b32_e32 v20, 16, v119
	v_and_b32_e32 v21, 0xffff0000, v119
	v_pk_fma_f32 v[20:21], v[12:13], v[160:161], v[20:21]
	v_pk_fma_f32 v[12:13], v[10:11], v[158:159], v[18:19]
	v_cvt_pk_bf16_f32 v10, v14, v15
	v_cvt_pk_bf16_f32 v11, v16, v17
	v_cvt_pk_bf16_f32 v12, v12, v13
	v_cvt_pk_bf16_f32 v13, v20, v21
	global_store_dwordx4 v[82:83], v[10:13], off offset:256
	s_waitcnt vmcnt(7)
	s_nop 0
	v_lshlrev_b32_e32 v10, 16, v76
	v_and_b32_e32 v11, 0xffff0000, v76
	v_lshlrev_b32_e32 v12, 16, v77
	v_and_b32_e32 v13, 0xffff0000, v77
	v_pk_fma_f32 v[8:9], v[8:9], v[164:165], v[12:13]
	v_pk_fma_f32 v[6:7], v[6:7], v[162:163], v[10:11]
	v_lshlrev_b32_e32 v10, 16, v78
	v_and_b32_e32 v11, 0xffff0000, v78
	v_lshlrev_b32_e32 v12, 16, v79
	v_and_b32_e32 v13, 0xffff0000, v79
	v_pk_fma_f32 v[12:13], v[4:5], v[160:161], v[12:13]
	v_pk_fma_f32 v[4:5], v[2:3], v[158:159], v[10:11]
	v_cvt_pk_bf16_f32 v2, v6, v7
	v_cvt_pk_bf16_f32 v3, v8, v9
	v_cvt_pk_bf16_f32 v4, v4, v5
	v_cvt_pk_bf16_f32 v5, v12, v13
	global_store_dwordx4 v[74:75], v[2:5], off offset:256
	s_cbranch_vccnz .LBB0_1593
	s_and_b64 vcc, exec, s[6:7]
	s_cbranch_vccnz .LBB0_1592
	s_barrier
	s_branch .LBB0_1592

.LBB0_1670:
	s_add_u32 s36, s34, 0xfffa8080
	s_addc_u32 s37, s35, -1
	s_add_i32 s60, 0, 0x10000
	s_cmp_eq_u32 s59, 18
	s_cselect_b32 s37, s27, s37
	s_cselect_b32 s36, s26, s36
	v_add_u32_e32 v0, s60, v143
	s_cselect_b32 s39, s29, s58
	s_cselect_b32 s38, s28, s31
	s_add_i32 s62, 0, 0x14000
	ds_read_b128 v[146:149], v0
	ds_read_b128 v[150:153], v0 offset:1024
	ds_read_b128 v[154:157], v0 offset:2048
	ds_read_b128 v[158:161], v0 offset:3072
	v_add_u32_e32 v0, s62, v143
	ds_read_b128 v[162:165], v0
	ds_read_b128 v[166:169], v0 offset:1024
	ds_read_b128 v[170:173], v0 offset:2048
	ds_read_b128 v[174:177], v0 offset:3072
	ds_read_b128 v[178:181], v145
	ds_read_b128 v[182:185], v145 offset:1024
	ds_read_b128 v[186:189], v145 offset:2048
	ds_read_b128 v[190:193], v145 offset:3072
	ds_read_b128 v[194:197], v145 offset:4096
	ds_read_b128 v[198:201], v145 offset:5120
	ds_read_b128 v[202:205], v145 offset:6144
	ds_read_b128 v[206:209], v145 offset:7168
	s_add_i32 m0, s85, 0xc000
	s_nop 0
	global_load_lds_dwordx4 v253, s[34:35]
	s_add_i32 m0, s85, 0xe000
	s_nop 0
	global_load_lds_dwordx4 v242, s[34:35]
	s_waitcnt vmcnt(8)
	s_waitcnt lgkmcnt(0)
	s_barrier
	s_setprio 1
	s_waitcnt lgkmcnt(0)
	v_mfma_scale_f32_16x16x128_f8f6f4 v[126:129], v[146:153], v[178:185], v[126:129], v234, v252 op_sel_hi:[0,0,0]
	v_mfma_scale_f32_16x16x128_f8f6f4 v[122:125], v[154:161], v[178:185], v[122:125], v234, v252 op_sel_hi:[0,0,0]
	v_mfma_scale_f32_16x16x128_f8f6f4 v[110:113], v[146:153], v[186:193], v[110:113], v234, v252 op_sel_hi:[0,0,0]
	v_mfma_scale_f32_16x16x128_f8f6f4 v[106:109], v[154:161], v[186:193], v[106:109], v234, v252 op_sel_hi:[0,0,0]
	v_mfma_scale_f32_16x16x128_f8f6f4 v[210:213], v[146:153], v[194:201], v[94:97], v234, v252 op_sel_hi:[0,0,0]
	v_mfma_scale_f32_16x16x128_f8f6f4 v[214:217], v[154:161], v[194:201], v[90:93], v234, v252 op_sel_hi:[0,0,0]
	v_mfma_scale_f32_16x16x128_f8f6f4 v[218:221], v[146:153], v[202:209], v[78:81], v234, v252 op_sel_hi:[0,0,0]
	v_mfma_scale_f32_16x16x128_f8f6f4 v[222:225], v[154:161], v[202:209], v[74:77], v234, v252 op_sel_hi:[0,0,0]
	s_setprio 0
	s_setprio 1
	v_mfma_scale_f32_16x16x128_f8f6f4 v[118:121], v[162:169], v[178:185], v[118:121], v234, v252 op_sel_hi:[0,0,0]
	v_mfma_scale_f32_16x16x128_f8f6f4 v[114:117], v[170:177], v[178:185], v[114:117], v234, v252 op_sel_hi:[0,0,0]
	v_mfma_scale_f32_16x16x128_f8f6f4 v[102:105], v[162:169], v[186:193], v[102:105], v234, v252 op_sel_hi:[0,0,0]
	v_mfma_scale_f32_16x16x128_f8f6f4 v[98:101], v[170:177], v[186:193], v[98:101], v234, v252 op_sel_hi:[0,0,0]
	v_mfma_scale_f32_16x16x128_f8f6f4 v[178:181], v[162:169], v[194:201], v[86:89], v234, v252 op_sel_hi:[0,0,0]
	v_mfma_scale_f32_16x16x128_f8f6f4 v[182:185], v[170:177], v[194:201], v[82:85], v234, v252 op_sel_hi:[0,0,0]
	v_mfma_scale_f32_16x16x128_f8f6f4 v[186:189], v[162:169], v[202:209], v[70:73], v234, v252 op_sel_hi:[0,0,0]
	v_mfma_scale_f32_16x16x128_f8f6f4 v[190:193], v[170:177], v[202:209], v[66:69], v234, v252 op_sel_hi:[0,0,0]
	s_setprio 0
	s_barrier
	s_add_i32 s60, s60, s33
	s_nop 2
	ds_read_b128 v[66:69], v145 offset:16384
	ds_read_b128 v[70:73], v145 offset:17408
	ds_read_b128 v[74:77], v145 offset:18432
	ds_read_b128 v[78:81], v145 offset:19456
	ds_read_b128 v[82:85], v145 offset:20480
	ds_read_b128 v[86:89], v145 offset:21504
	ds_read_b128 v[90:93], v145 offset:22528
	ds_read_b128 v[94:97], v145 offset:23552
	s_mov_b32 m0, s60
	s_nop 0
	global_load_lds_dwordx4 v243, s[38:39]
	s_add_i32 m0, s60, 0x2000
	s_add_u32 s60, s38, 0x58000
	global_load_lds_dwordx4 v142, s[38:39]
	s_addc_u32 s61, s39, 0
	s_add_i32 s62, s62, s33
	s_mov_b32 m0, s62
	s_nop 0
	global_load_lds_dwordx4 v243, s[60:61]
	s_add_i32 m0, s62, 0x2000
	s_nop 0
	global_load_lds_dwordx4 v142, s[60:61]
	s_waitcnt vmcnt(6)
	s_waitcnt lgkmcnt(0)
	s_barrier
	s_setprio 1
	s_waitcnt lgkmcnt(0)
	v_mfma_scale_f32_16x16x128_f8f6f4 v[62:65], v[146:153], v[66:73], v[62:65], v234, v252 op_sel_hi:[0,0,0]
	v_mfma_scale_f32_16x16x128_f8f6f4 v[58:61], v[154:161], v[66:73], v[58:61], v234, v252 op_sel_hi:[0,0,0]
	v_mfma_scale_f32_16x16x128_f8f6f4 v[54:57], v[146:153], v[74:81], v[54:57], v234, v252 op_sel_hi:[0,0,0]
	v_mfma_scale_f32_16x16x128_f8f6f4 v[194:197], v[154:161], v[74:81], v[46:49], v234, v252 op_sel_hi:[0,0,0]
	v_mfma_scale_f32_16x16x128_f8f6f4 v[198:201], v[146:153], v[82:89], v[38:41], v234, v252 op_sel_hi:[0,0,0]
	v_mfma_scale_f32_16x16x128_f8f6f4 v[202:205], v[154:161], v[82:89], v[30:33], v234, v252 op_sel_hi:[0,0,0]
	v_mfma_scale_f32_16x16x128_f8f6f4 v[206:209], v[146:153], v[90:97], v[22:25], v234, v252 op_sel_hi:[0,0,0]
	v_mfma_scale_f32_16x16x128_f8f6f4 v[226:229], v[154:161], v[90:97], v[14:17], v234, v252 op_sel_hi:[0,0,0]
	s_setprio 0
	s_setprio 1
	v_mfma_scale_f32_16x16x128_f8f6f4 v[50:53], v[162:169], v[66:73], v[50:53], v234, v252 op_sel_hi:[0,0,0]
	v_mfma_scale_f32_16x16x128_f8f6f4 v[244:247], v[170:177], v[66:73], v[42:45], v234, v252 op_sel_hi:[0,0,0]
	v_mfma_scale_f32_16x16x128_f8f6f4 v[248:251], v[162:169], v[74:81], v[34:37], v234, v252 op_sel_hi:[0,0,0]
	v_mfma_scale_f32_16x16x128_f8f6f4 v[236:239], v[170:177], v[74:81], v[26:29], v234, v252 op_sel_hi:[0,0,0]
	v_mfma_scale_f32_16x16x128_f8f6f4 v[230:233], v[162:169], v[82:89], v[18:21], v234, v252 op_sel_hi:[0,0,0]
	v_mfma_scale_f32_16x16x128_f8f6f4 v[130:133], v[170:177], v[82:89], v[10:13], v234, v252 op_sel_hi:[0,0,0]
	v_mfma_scale_f32_16x16x128_f8f6f4 v[134:137], v[162:169], v[90:97], v[6:9], v234, v252 op_sel_hi:[0,0,0]
	v_mfma_scale_f32_16x16x128_f8f6f4 v[138:141], v[170:177], v[90:97], v[2:5], v234, v252 op_sel_hi:[0,0,0]
	s_setprio 0
	s_barrier
	s_add_i32 s62, 0, 0x18000
	v_add_u32_e32 v0, s62, v143
	s_add_i32 s63, 0, 0x1c000
	s_nop 1
	ds_read_b128 v[2:5], v0
	ds_read_b128 v[6:9], v0 offset:1024
	ds_read_b128 v[10:13], v0 offset:2048
	ds_read_b128 v[14:17], v0 offset:3072
	v_add_u32_e32 v0, s63, v143
	ds_read_b128 v[146:149], v0
	ds_read_b128 v[150:153], v0 offset:1024
	ds_read_b128 v[154:157], v0 offset:2048
	ds_read_b128 v[158:161], v0 offset:3072
	s_add_u32 s60, s36, 0x58000
	ds_read_b128 v[18:21], v145 offset:32768
	ds_read_b128 v[22:25], v145 offset:33792
	ds_read_b128 v[26:29], v145 offset:34816
	ds_read_b128 v[30:33], v145 offset:35840
	ds_read_b128 v[34:37], v145 offset:36864
	ds_read_b128 v[38:41], v145 offset:37888
	ds_read_b128 v[42:45], v145 offset:38912
	ds_read_b128 v[46:49], v145 offset:39936
	s_addc_u32 s61, s37, 0
	s_mov_b32 m0, s85
	s_nop 0
	global_load_lds_dwordx4 v253, s[36:37]
	s_mov_b32 m0, s50
	s_nop 0
	global_load_lds_dwordx4 v242, s[36:37]
	s_mov_b32 m0, s51
	s_nop 0
	global_load_lds_dwordx4 v253, s[60:61]
	s_mov_b32 m0, s52
	s_nop 0
	global_load_lds_dwordx4 v242, s[60:61]
	s_waitcnt vmcnt(8)
	s_waitcnt lgkmcnt(0)
	s_barrier
	s_setprio 1
	s_waitcnt lgkmcnt(0)
	v_mfma_scale_f32_16x16x128_f8f6f4 v[126:129], v[2:9], v[18:25], v[126:129], v234, v252 op_sel_hi:[0,0,0]
	v_mfma_scale_f32_16x16x128_f8f6f4 v[122:125], v[10:17], v[18:25], v[122:125], v234, v252 op_sel_hi:[0,0,0]
	v_mfma_scale_f32_16x16x128_f8f6f4 v[110:113], v[2:9], v[26:33], v[110:113], v234, v252 op_sel_hi:[0,0,0]
	v_mfma_scale_f32_16x16x128_f8f6f4 v[106:109], v[10:17], v[26:33], v[106:109], v234, v252 op_sel_hi:[0,0,0]
	v_mfma_scale_f32_16x16x128_f8f6f4 v[94:97], v[2:9], v[34:41], v[210:213], v234, v252 op_sel_hi:[0,0,0]
	v_mfma_scale_f32_16x16x128_f8f6f4 v[90:93], v[10:17], v[34:41], v[214:217], v234, v252 op_sel_hi:[0,0,0]
	v_mfma_scale_f32_16x16x128_f8f6f4 v[78:81], v[2:9], v[42:49], v[218:221], v234, v252 op_sel_hi:[0,0,0]
	v_mfma_scale_f32_16x16x128_f8f6f4 v[74:77], v[10:17], v[42:49], v[222:225], v234, v252 op_sel_hi:[0,0,0]
	s_setprio 0
	s_setprio 1
	v_mfma_scale_f32_16x16x128_f8f6f4 v[118:121], v[146:153], v[18:25], v[118:121], v234, v252 op_sel_hi:[0,0,0]
	v_mfma_scale_f32_16x16x128_f8f6f4 v[114:117], v[154:161], v[18:25], v[114:117], v234, v252 op_sel_hi:[0,0,0]
	v_mfma_scale_f32_16x16x128_f8f6f4 v[102:105], v[146:153], v[26:33], v[102:105], v234, v252 op_sel_hi:[0,0,0]
	v_mfma_scale_f32_16x16x128_f8f6f4 v[98:101], v[154:161], v[26:33], v[98:101], v234, v252 op_sel_hi:[0,0,0]
	v_mfma_scale_f32_16x16x128_f8f6f4 v[86:89], v[146:153], v[34:41], v[178:181], v234, v252 op_sel_hi:[0,0,0]
	v_mfma_scale_f32_16x16x128_f8f6f4 v[82:85], v[154:161], v[34:41], v[182:185], v234, v252 op_sel_hi:[0,0,0]
	v_mfma_scale_f32_16x16x128_f8f6f4 v[70:73], v[146:153], v[42:49], v[186:189], v234, v252 op_sel_hi:[0,0,0]
	v_mfma_scale_f32_16x16x128_f8f6f4 v[66:69], v[154:161], v[42:49], v[190:193], v234, v252 op_sel_hi:[0,0,0]
	s_setprio 0
	s_barrier
	v_mov_b32_e32 v0, v243
	ds_read_b128 v[162:165], v145 offset:49152
	ds_read_b128 v[166:169], v145 offset:50176
	ds_read_b128 v[170:173], v145 offset:51200
	ds_read_b128 v[174:177], v145 offset:52224
	ds_read_b128 v[178:181], v145 offset:53248
	ds_read_b128 v[182:185], v145 offset:54272
	ds_read_b128 v[186:189], v145 offset:55296
	ds_read_b128 v[190:193], v145 offset:56320
	s_add_i32 s60, s62, s33
	v_lshl_add_u64 v[18:19], s[38:39], 0, v[0:1]
	v_lshl_add_u64 v[18:19], v[18:19], 0, s[90:91]
	s_mov_b32 m0, s60
	v_mov_b32_e32 v0, v142
	global_load_lds_dwordx4 v[18:19], off
	s_add_i32 m0, s60, 0x2000
	s_nop 0
	v_lshl_add_u64 v[18:19], s[38:39], 0, v[0:1]
	s_add_u32 s38, s38, 0x58080
	v_lshl_add_u64 v[18:19], v[18:19], 0, s[90:91]
	s_addc_u32 s39, s39, 0
	s_add_i32 s60, s63, s33
	global_load_lds_dwordx4 v[18:19], off
	s_mov_b32 m0, s60
	s_nop 0
	global_load_lds_dwordx4 v243, s[38:39]
	s_add_i32 m0, s60, 0x2000
	s_nop 0
	global_load_lds_dwordx4 v142, s[38:39]
	s_waitcnt vmcnt(6)
	s_waitcnt lgkmcnt(0)
	s_barrier
	s_setprio 1
	s_waitcnt lgkmcnt(0)
	v_mfma_scale_f32_16x16x128_f8f6f4 v[62:65], v[2:9], v[162:169], v[62:65], v234, v252 op_sel_hi:[0,0,0]
	v_mfma_scale_f32_16x16x128_f8f6f4 v[58:61], v[10:17], v[162:169], v[58:61], v234, v252 op_sel_hi:[0,0,0]
	v_mfma_scale_f32_16x16x128_f8f6f4 v[54:57], v[2:9], v[170:177], v[54:57], v234, v252 op_sel_hi:[0,0,0]
	v_mfma_scale_f32_16x16x128_f8f6f4 v[46:49], v[10:17], v[170:177], v[194:197], v234, v252 op_sel_hi:[0,0,0]
	v_mfma_scale_f32_16x16x128_f8f6f4 v[38:41], v[2:9], v[178:185], v[198:201], v234, v252 op_sel_hi:[0,0,0]
	v_mfma_scale_f32_16x16x128_f8f6f4 v[30:33], v[10:17], v[178:185], v[202:205], v234, v252 op_sel_hi:[0,0,0]
	v_mfma_scale_f32_16x16x128_f8f6f4 v[22:25], v[2:9], v[186:193], v[206:209], v234, v252 op_sel_hi:[0,0,0]
	v_mfma_scale_f32_16x16x128_f8f6f4 v[14:17], v[10:17], v[186:193], v[226:229], v234, v252 op_sel_hi:[0,0,0]
	s_setprio 0
	s_setprio 1
	v_mfma_scale_f32_16x16x128_f8f6f4 v[50:53], v[146:153], v[162:169], v[50:53], v234, v252 op_sel_hi:[0,0,0]
	v_mfma_scale_f32_16x16x128_f8f6f4 v[42:45], v[154:161], v[162:169], v[244:247], v234, v252 op_sel_hi:[0,0,0]
	v_mfma_scale_f32_16x16x128_f8f6f4 v[34:37], v[146:153], v[170:177], v[248:251], v234, v252 op_sel_hi:[0,0,0]
	v_mfma_scale_f32_16x16x128_f8f6f4 v[26:29], v[154:161], v[170:177], v[236:239], v234, v252 op_sel_hi:[0,0,0]
	v_mfma_scale_f32_16x16x128_f8f6f4 v[18:21], v[146:153], v[178:185], v[230:233], v234, v252 op_sel_hi:[0,0,0]
	v_mfma_scale_f32_16x16x128_f8f6f4 v[10:13], v[154:161], v[178:185], v[130:133], v234, v252 op_sel_hi:[0,0,0]
	v_mfma_scale_f32_16x16x128_f8f6f4 v[6:9], v[146:153], v[186:193], v[134:137], v234, v252 op_sel_hi:[0,0,0]
	v_mfma_scale_f32_16x16x128_f8f6f4 v[2:5], v[154:161], v[186:193], v[138:141], v234, v252 op_sel_hi:[0,0,0]
	s_setprio 0
	s_barrier
	v_mov_b32_e32 v0, v253
	s_mov_b32 m0, s53
	v_lshl_add_u64 v[198:199], s[36:37], 0, v[0:1]
	v_lshl_add_u64 v[198:199], v[198:199], 0, s[90:91]
	v_mov_b32_e32 v0, v242
	global_load_lds_dwordx4 v[198:199], off
	s_mov_b32 m0, s54
	v_lshl_add_u64 v[198:199], s[36:37], 0, v[0:1]
	v_lshl_add_u64 v[198:199], v[198:199], 0, s[90:91]
	global_load_lds_dwordx4 v[198:199], off
	s_add_i32 s59, s59, 2
	s_add_u32 s34, s34, 0x100
	s_addc_u32 s35, s35, 0
	s_add_u32 s31, s31, 0x100
	s_addc_u32 s58, s58, 0
	s_cmp_gt_u32 s59, 19
	s_cbranch_scc0 .LBB0_1670
	v_readlane_b32 s34, v254, 19
	v_readlane_b32 s35, v254, 20
	s_and_b64 vcc, exec, s[34:35]
	s_lshl_b32 s30, s30, 8
	s_add_i32 s30, s30, s87
	v_mbcnt_lo_u32_b32 v0, -1, 0
	v_mbcnt_hi_u32_b32 v0, -1, v0
	v_readlane_b32 s34, v254, 55
	v_and_or_b32 v146, v0, 15, s30
	v_ashrrev_i32_e32 v147, 31, v146
	v_lshl_add_u64 v[130:131], v[146:147], 2, s[14:15]
	global_load_dword v148, v[130:131], off
	global_load_dword v150, v[130:131], off offset:64
	global_load_dword v144, v[130:131], off offset:128
	global_load_dword v140, v[130:131], off offset:192
	global_load_dword v138, v[130:131], off offset:512
	global_load_dword v136, v[130:131], off offset:576
	global_load_dword v132, v[130:131], off offset:640
	s_nop 0
	global_load_dword v130, v[130:131], off offset:704
	s_cbranch_vccz .LBB0_1673
	s_barrier
.LBB0_1673:
	s_lshl_b32 s30, s57, 8
	s_ashr_i32 s31, s30, 31
	v_lshlrev_b64 v[134:135], 11, v[146:147]
	v_lshl_add_u64 v[134:135], s[20:21], 0, v[134:135]
	s_lshl_b64 s[30:31], s[30:31], 1
	v_readlane_b32 s35, v254, 56
	v_lshl_add_u64 v[134:135], v[134:135], 0, s[30:31]
	s_mov_b32 s35, s95
	v_lshl_add_u64 v[134:135], v[134:135], 0, s[34:35]
	v_and_b32_e32 v0, 48, v0
	v_lshl_add_u64 v[134:135], v[134:135], 0, v[0:1]
	s_mov_b64 s[58:59], 0x2000
	v_mov_b32_e32 v236, 0x3a800000
	s_waitcnt vmcnt(0)
	v_pk_mul_f32 v[128:129], v[128:129], v[148:149] op_sel_hi:[1,0]
	v_pk_mul_f32 v[126:127], v[126:127], v[148:149] op_sel_hi:[1,0]
	v_pk_mul_f32 v[152:153], v[124:125], v[148:149] op_sel_hi:[1,0]
	v_pk_mul_f32 v[124:125], v[122:123], v[148:149] op_sel_hi:[1,0]
	v_cvt_pk_bf16_f32 v122, v126, v127
	v_cvt_pk_bf16_f32 v123, v128, v129
	v_cvt_pk_bf16_f32 v124, v124, v125
	v_cvt_pk_bf16_f32 v125, v152, v153
	global_store_dwordx4 v[134:135], v[122:125], off
	v_pk_mul_f32 v[120:121], v[120:121], v[148:149] op_sel_hi:[1,0]
	v_pk_mul_f32 v[118:119], v[118:119], v[148:149] op_sel_hi:[1,0]
	v_pk_mul_f32 v[122:123], v[116:117], v[148:149] op_sel_hi:[1,0]
	v_pk_mul_f32 v[116:117], v[114:115], v[148:149] op_sel_hi:[1,0]
	v_cvt_pk_bf16_f32 v114, v118, v119
	v_cvt_pk_bf16_f32 v115, v120, v121
	v_cvt_pk_bf16_f32 v116, v116, v117
	v_cvt_pk_bf16_f32 v117, v122, v123
	global_store_dwordx4 v[134:135], v[114:117], off offset:256
	v_pk_mul_f32 v[112:113], v[112:113], v[150:151] op_sel_hi:[1,0]
	v_pk_mul_f32 v[110:111], v[110:111], v[150:151] op_sel_hi:[1,0]
	v_or_b32_e32 v114, 16, v146
	v_ashrrev_i32_e32 v115, 31, v114
	v_lshlrev_b64 v[114:115], 11, v[114:115]
	v_lshl_add_u64 v[114:115], s[20:21], 0, v[114:115]
	v_lshl_add_u64 v[114:115], v[114:115], 0, s[30:31]
	v_lshl_add_u64 v[114:115], v[114:115], 0, s[34:35]
	v_pk_mul_f32 v[116:117], v[108:109], v[150:151] op_sel_hi:[1,0]
	v_pk_mul_f32 v[108:109], v[106:107], v[150:151] op_sel_hi:[1,0]
	v_lshl_add_u64 v[114:115], v[114:115], 0, v[0:1]
	v_cvt_pk_bf16_f32 v106, v110, v111
	v_cvt_pk_bf16_f32 v107, v112, v113
	v_cvt_pk_bf16_f32 v108, v108, v109
	v_cvt_pk_bf16_f32 v109, v116, v117
	global_store_dwordx4 v[114:115], v[106:109], off
	v_pk_mul_f32 v[104:105], v[104:105], v[150:151] op_sel_hi:[1,0]
	v_pk_mul_f32 v[102:103], v[102:103], v[150:151] op_sel_hi:[1,0]
	v_pk_mul_f32 v[106:107], v[100:101], v[150:151] op_sel_hi:[1,0]
	v_pk_mul_f32 v[100:101], v[98:99], v[150:151] op_sel_hi:[1,0]
	v_cvt_pk_bf16_f32 v98, v102, v103
	v_cvt_pk_bf16_f32 v99, v104, v105
	v_cvt_pk_bf16_f32 v100, v100, v101
	v_cvt_pk_bf16_f32 v101, v106, v107
	global_store_dwordx4 v[114:115], v[98:101], off offset:256
	v_pk_mul_f32 v[96:97], v[96:97], v[144:145] op_sel_hi:[1,0]
	v_pk_mul_f32 v[94:95], v[94:95], v[144:145] op_sel_hi:[1,0]
	v_or_b32_e32 v98, 32, v146
	v_ashrrev_i32_e32 v99, 31, v98
	v_lshlrev_b64 v[98:99], 11, v[98:99]
	v_lshl_add_u64 v[98:99], s[20:21], 0, v[98:99]
	v_lshl_add_u64 v[98:99], v[98:99], 0, s[30:31]
	v_lshl_add_u64 v[98:99], v[98:99], 0, s[34:35]
	v_pk_mul_f32 v[100:101], v[92:93], v[144:145] op_sel_hi:[1,0]
	v_pk_mul_f32 v[92:93], v[90:91], v[144:145] op_sel_hi:[1,0]
	v_lshl_add_u64 v[98:99], v[98:99], 0, v[0:1]
	v_cvt_pk_bf16_f32 v90, v94, v95
	v_cvt_pk_bf16_f32 v91, v96, v97
	v_cvt_pk_bf16_f32 v92, v92, v93
	v_cvt_pk_bf16_f32 v93, v100, v101
	global_store_dwordx4 v[98:99], v[90:93], off
	v_pk_mul_f32 v[88:89], v[88:89], v[144:145] op_sel_hi:[1,0]
	v_pk_mul_f32 v[86:87], v[86:87], v[144:145] op_sel_hi:[1,0]
	v_pk_mul_f32 v[90:91], v[84:85], v[144:145] op_sel_hi:[1,0]
	v_pk_mul_f32 v[84:85], v[82:83], v[144:145] op_sel_hi:[1,0]
	v_cvt_pk_bf16_f32 v82, v86, v87
	v_cvt_pk_bf16_f32 v83, v88, v89
	v_cvt_pk_bf16_f32 v84, v84, v85
	v_cvt_pk_bf16_f32 v85, v90, v91
	global_store_dwordx4 v[98:99], v[82:85], off offset:256
	v_pk_mul_f32 v[80:81], v[80:81], v[140:141] op_sel_hi:[1,0]
	v_pk_mul_f32 v[78:79], v[78:79], v[140:141] op_sel_hi:[1,0]
	v_or_b32_e32 v82, 48, v146
	v_ashrrev_i32_e32 v83, 31, v82
	v_lshlrev_b64 v[82:83], 11, v[82:83]
	v_lshl_add_u64 v[82:83], s[20:21], 0, v[82:83]
	v_lshl_add_u64 v[82:83], v[82:83], 0, s[30:31]
	v_lshl_add_u64 v[82:83], v[82:83], 0, s[34:35]
	v_pk_mul_f32 v[84:85], v[76:77], v[140:141] op_sel_hi:[1,0]
	v_pk_mul_f32 v[76:77], v[74:75], v[140:141] op_sel_hi:[1,0]
	s_mov_b32 s30, s34
	v_lshl_add_u64 v[82:83], v[82:83], 0, v[0:1]
	v_cvt_pk_bf16_f32 v74, v78, v79
	v_cvt_pk_bf16_f32 v75, v80, v81
	v_cvt_pk_bf16_f32 v76, v76, v77
	v_cvt_pk_bf16_f32 v77, v84, v85
	v_writelane_b32 v254, s30, 55
	global_store_dwordx4 v[82:83], v[74:77], off
	v_pk_mul_f32 v[72:73], v[72:73], v[140:141] op_sel_hi:[1,0]
	v_pk_mul_f32 v[70:71], v[70:71], v[140:141] op_sel_hi:[1,0]
	v_pk_mul_f32 v[74:75], v[68:69], v[140:141] op_sel_hi:[1,0]
	v_pk_mul_f32 v[68:69], v[66:67], v[140:141] op_sel_hi:[1,0]
	v_writelane_b32 v254, s31, 56
	v_cvt_pk_bf16_f32 v66, v70, v71
	v_cvt_pk_bf16_f32 v67, v72, v73
	v_cvt_pk_bf16_f32 v68, v68, v69
	v_cvt_pk_bf16_f32 v69, v74, v75
	s_mov_b64 s[30:31], 0x40000
	global_store_dwordx4 v[82:83], v[66:69], off offset:256
	v_pk_mul_f32 v[62:63], v[62:63], v[138:139] op_sel_hi:[1,0]
	v_pk_mul_f32 v[64:65], v[64:65], v[138:139] op_sel_hi:[1,0]
	v_lshl_add_u64 v[66:67], v[134:135], 0, s[30:31]
	s_mov_b32 s30, 0x40000
	v_pk_mul_f32 v[68:69], v[60:61], v[138:139] op_sel_hi:[1,0]
	v_pk_mul_f32 v[60:61], v[58:59], v[138:139] op_sel_hi:[1,0]
	v_cvt_pk_bf16_f32 v58, v62, v63
	v_add_co_u32_e32 v62, vcc, s30, v134
	v_cvt_pk_bf16_f32 v59, v64, v65
	v_cvt_pk_bf16_f32 v60, v60, v61
	v_cvt_pk_bf16_f32 v61, v68, v69
	v_addc_co_u32_e32 v63, vcc, 0, v135, vcc
	global_store_dwordx4 v[62:63], v[58:61], off
	v_pk_mul_f32 v[52:53], v[52:53], v[138:139] op_sel_hi:[1,0]
	v_pk_mul_f32 v[50:51], v[50:51], v[138:139] op_sel_hi:[1,0]
	v_pk_mul_f32 v[58:59], v[44:45], v[138:139] op_sel_hi:[1,0]
	v_pk_mul_f32 v[44:45], v[42:43], v[138:139] op_sel_hi:[1,0]
	v_cvt_pk_bf16_f32 v42, v50, v51
	v_cvt_pk_bf16_f32 v43, v52, v53
	v_cvt_pk_bf16_f32 v44, v44, v45
	v_cvt_pk_bf16_f32 v45, v58, v59
	s_mov_b64 s[30:31], 0x48000
	global_store_dwordx4 v[66:67], v[42:45], off offset:256
	v_lshl_add_u64 v[50:51], v[134:135], 0, s[30:31]
	v_pk_mul_f32 v[46:47], v[46:47], v[136:137] op_sel_hi:[1,0]
	v_pk_mul_f32 v[44:45], v[56:57], v[136:137] op_sel_hi:[1,0]
	v_pk_mul_f32 v[42:43], v[54:55], v[136:137] op_sel_hi:[1,0]
	s_mov_b32 s30, 0x48000
	v_pk_mul_f32 v[48:49], v[48:49], v[136:137] op_sel_hi:[1,0]
	v_cvt_pk_bf16_f32 v42, v42, v43
	v_cvt_pk_bf16_f32 v43, v44, v45
	v_cvt_pk_bf16_f32 v44, v46, v47
	v_add_co_u32_e32 v46, vcc, s30, v134
	v_cvt_pk_bf16_f32 v45, v48, v49
	s_nop 0
	v_addc_co_u32_e32 v47, vcc, 0, v135, vcc
	global_store_dwordx4 v[46:47], v[42:45], off
	v_pk_mul_f32 v[36:37], v[36:37], v[136:137] op_sel_hi:[1,0]
	v_pk_mul_f32 v[34:35], v[34:35], v[136:137] op_sel_hi:[1,0]
	v_pk_mul_f32 v[42:43], v[28:29], v[136:137] op_sel_hi:[1,0]
	v_pk_mul_f32 v[28:29], v[26:27], v[136:137] op_sel_hi:[1,0]
	v_cvt_pk_bf16_f32 v26, v34, v35
	v_cvt_pk_bf16_f32 v27, v36, v37
	v_cvt_pk_bf16_f32 v28, v28, v29
	v_cvt_pk_bf16_f32 v29, v42, v43
	s_mov_b64 s[30:31], 0x50000
	global_store_dwordx4 v[50:51], v[26:29], off offset:256
	v_lshl_add_u64 v[34:35], v[134:135], 0, s[30:31]
	v_pk_mul_f32 v[30:31], v[30:31], v[132:133] op_sel_hi:[1,0]
	v_pk_mul_f32 v[28:29], v[40:41], v[132:133] op_sel_hi:[1,0]
	v_pk_mul_f32 v[26:27], v[38:39], v[132:133] op_sel_hi:[1,0]
	s_mov_b32 s30, 0x50000
	v_pk_mul_f32 v[32:33], v[32:33], v[132:133] op_sel_hi:[1,0]
	v_cvt_pk_bf16_f32 v26, v26, v27
	v_cvt_pk_bf16_f32 v27, v28, v29
	v_cvt_pk_bf16_f32 v28, v30, v31
	v_add_co_u32_e32 v30, vcc, s30, v134
	v_cvt_pk_bf16_f32 v29, v32, v33
	s_nop 0
	v_addc_co_u32_e32 v31, vcc, 0, v135, vcc
	global_store_dwordx4 v[30:31], v[26:29], off
	v_pk_mul_f32 v[20:21], v[20:21], v[132:133] op_sel_hi:[1,0]
	v_pk_mul_f32 v[18:19], v[18:19], v[132:133] op_sel_hi:[1,0]
	v_pk_mul_f32 v[26:27], v[12:13], v[132:133] op_sel_hi:[1,0]
	v_pk_mul_f32 v[12:13], v[10:11], v[132:133] op_sel_hi:[1,0]
	v_cvt_pk_bf16_f32 v10, v18, v19
	v_cvt_pk_bf16_f32 v11, v20, v21
	v_cvt_pk_bf16_f32 v12, v12, v13
	v_cvt_pk_bf16_f32 v13, v26, v27
	s_mov_b64 s[30:31], 0x58000
	global_store_dwordx4 v[34:35], v[10:13], off offset:256
	v_lshl_add_u64 v[18:19], v[134:135], 0, s[30:31]
	v_pk_mul_f32 v[14:15], v[14:15], v[130:131] op_sel_hi:[1,0]
	v_pk_mul_f32 v[12:13], v[24:25], v[130:131] op_sel_hi:[1,0]
	v_pk_mul_f32 v[10:11], v[22:23], v[130:131] op_sel_hi:[1,0]
	s_mov_b32 s30, 0x58000
	v_pk_mul_f32 v[16:17], v[16:17], v[130:131] op_sel_hi:[1,0]
	v_cvt_pk_bf16_f32 v10, v10, v11
	v_cvt_pk_bf16_f32 v11, v12, v13
	v_cvt_pk_bf16_f32 v12, v14, v15
	v_add_co_u32_e32 v14, vcc, s30, v134
	v_cvt_pk_bf16_f32 v13, v16, v17
	s_nop 0
	v_addc_co_u32_e32 v15, vcc, 0, v135, vcc
	global_store_dwordx4 v[14:15], v[10:13], off
	v_pk_mul_f32 v[8:9], v[8:9], v[130:131] op_sel_hi:[1,0]
	v_pk_mul_f32 v[6:7], v[6:7], v[130:131] op_sel_hi:[1,0]
	v_pk_mul_f32 v[10:11], v[4:5], v[130:131] op_sel_hi:[1,0]
	v_pk_mul_f32 v[4:5], v[2:3], v[130:131] op_sel_hi:[1,0]
	v_cvt_pk_bf16_f32 v2, v6, v7
	v_cvt_pk_bf16_f32 v3, v8, v9
	v_cvt_pk_bf16_f32 v4, v4, v5
	v_cvt_pk_bf16_f32 v5, v10, v11
	s_mov_b64 s[30:31], -1
	s_and_b64 vcc, exec, s[8:9]
	global_store_dwordx4 v[18:19], v[2:5], off offset:256
	s_cbranch_vccnz .LBB0_1651
	s_and_b64 vcc, exec, s[6:7]
	s_cbranch_vccnz .LBB0_1650
	s_barrier
	s_branch .LBB0_1650
